# S2 layer-0 epilogue: all sixteen u2 tile loads issued up front into dead registers, one wait
# baseline (speedup 1.0000x reference)
; #define GAS __attribute__((address_space(1)))
; __device__ __forceinline__ float gelu_tanh(float y) { const float a = 1.5957691216f * (y + 0.044715f * y * y * y); return y * sigmoidf_(a); }
; __device__ __forceinline__ unsigned cvt_pk_bf16(float lo, float hi) { unsigned r; asm volatile("v_cvt_pk_bf16_f32 %0, %1, %2" : "=v"(r) : "v"(lo), "v"(hi)); return r; }
;     __device__ __forceinline__ void operator()(const f32x4 (&acc)[2][2][4][2], const Unit& u, int wr, int wc, int fr, int fq) const {
;         const int g = u.aux, inst0 = u.pm * 256 + wr * 64 + fr, c0 = u.pn * 256 + wc * 32 + 8 * fq;
; #pragma unroll
;         for (int bj = 0; bj < 2; ++bj) { const int cidx = c0 + bj * 128, t = cidx >> 4, o0 = cidx & 15;
;             const f32x4 d0 = *(const GAS f32x4*)(dsk + g * 16 + o0), d1 = *(const GAS f32x4*)(dsk + g * 16 + o0 + 4);
; #pragma unroll
;             for (int ai = 0; ai < 2; ++ai)
; #pragma unroll
;                 for (int m = 0; m < 4; ++m) { const int inst = inst0 + ai * 128 + m * 16;
;                     if (inst < MT / 64) {
;                         const v4u uu = *(const GAS v4u*)(u2 + ((size_t)(g * NINST + inst) * KS2 + cidx));
;                         const f32x4 a0 = acc[ai][bj][m][0] * S5_INV, a1 = acc[ai][bj][m][1] * S5_INV;
;                         const float y0 = a0[0] + d0[0] * bflo(uu.x), y1 = a0[1] + d0[1] * bfhi(uu.x), y2 = a0[2] + d0[2] * bflo(uu.y), y3 = a0[3] + d0[3] * bfhi(uu.y);
;                         const float y4 = a1[0] + d1[0] * bflo(uu.z), y5 = a1[1] + d1[1] * bfhi(uu.z), y6 = a1[2] + d1[2] * bflo(uu.w), y7 = a1[3] + d1[3] * bfhi(uu.w);
;                         v4u w; w.x = pg8::cvt_pk_bf16(gelu_tanh(y0), gelu_tanh(y1)); w.y = pg8::cvt_pk_bf16(gelu_tanh(y2), gelu_tanh(y3));
;                         w.z = pg8::cvt_pk_bf16(gelu_tanh(y4), gelu_tanh(y5)); w.w = pg8::cvt_pk_bf16(gelu_tanh(y6), gelu_tanh(y7));
;                         *(GAS v4u*)(z + ((size_t)(inst * 64 + t) * DSSM + g * 16 + o0)) = w; } } }
.LBB0_542:
	s_lshl_b32 s2, s14, 4
	s_ashr_i32 s3, s2, 31
	v_lshl_add_u64 v[12:13], s[2:3], 2, v[174:175]
	global_load_dwordx4 v[6:9], v[12:13], off
	global_load_dwordx4 v[2:5], v[12:13], off offset:16
	v_lshl_or_b32 v10, s12, 8, v188
	v_lshl_add_u32 v14, s13, 8, v1
	s_lshl_b32 s20, s14, 9
	v_ashrrev_i32_e32 v29, 4, v10
	v_ashrrev_i32_e32 v11, 31, v10
	v_cmp_gt_i32_e32 vcc, s65, v14
	v_add_u32_e32 v22, s20, v14
	v_lshlrev_b32_e32 v170, 1, v172
	v_mul_lo_u32 v255, v22, s66
	v_lshl_add_u32 v255, v10, 1, v255
	s_add_u32 s98, s22, 0x0
	s_addc_u32 s99, s23, 0
	global_load_dwordx4 v[196:199], v255, s[98:99]
	s_add_u32 s98, s22, 0xa000
	s_addc_u32 s99, s23, 0
	global_load_dwordx4 v[200:203], v255, s[98:99]
	s_add_u32 s98, s22, 0x14000
	s_addc_u32 s99, s23, 0
	global_load_dwordx4 v[204:207], v255, s[98:99]
	s_add_u32 s98, s22, 0x1e000
	s_addc_u32 s99, s23, 0
	global_load_dwordx4 v[208:211], v255, s[98:99]
	s_add_u32 s98, s22, 0x50000
	s_addc_u32 s99, s23, 0
	global_load_dwordx4 v[212:215], v255, s[98:99]
	s_add_u32 s98, s22, 0x5a000
	s_addc_u32 s99, s23, 0
	global_load_dwordx4 v[216:219], v255, s[98:99]
	s_add_u32 s98, s22, 0x64000
	s_addc_u32 s99, s23, 0
	global_load_dwordx4 v[220:223], v255, s[98:99]
	s_add_u32 s98, s22, 0x6e000
	s_addc_u32 s99, s23, 0
	global_load_dwordx4 v[224:227], v255, s[98:99]
	s_add_u32 s98, s22, 0x100
	s_addc_u32 s99, s23, 0
	global_load_dwordx4 v[228:231], v255, s[98:99]
	s_add_u32 s98, s22, 0x14100
	s_addc_u32 s99, s23, 0
	global_load_dwordx4 v[232:235], v255, s[98:99]
	s_add_u32 s98, s22, 0x50100
	s_addc_u32 s99, s23, 0
	global_load_dwordx4 v[240:243], v255, s[98:99]
	s_add_u32 s98, s22, 0x64100
	s_addc_u32 s99, s23, 0
	global_load_dwordx4 v[244:247], v255, s[98:99]
	s_add_u32 s98, s22, 0xa100
	s_addc_u32 s99, s23, 0
	global_load_dwordx4 v[162:165], v255, s[98:99]
	s_add_u32 s98, s22, 0x1e100
	s_addc_u32 s99, s23, 0
	global_load_dwordx4 v[166:169], v255, s[98:99]
	s_add_u32 s98, s22, 0x5a100
	s_addc_u32 s99, s23, 0
	global_load_dwordx4 v[176:179], v255, s[98:99]
	s_add_u32 s98, s22, 0x6e100
	s_addc_u32 s99, s23, 0
	global_load_dwordx4 v[250:253], v255, s[98:99]
	s_waitcnt vmcnt(0)
	s_and_saveexec_b64 s[4:5], vcc
	s_cbranch_execz .LBB0_544
	v_mov_b64_e32 v[16:17], s[22:23]
	v_mad_i64_i32 v[16:17], s[6:7], v22, s66, v[16:17]
	v_lshl_add_u64 v[16:17], v[10:11], 1, v[16:17]
	v_mov_b64_e32 v[16:17], v[196:197]
	v_mov_b64_e32 v[18:19], v[198:199]
	v_pk_mul_f32 v[20:21], v[160:161], s[36:37] op_sel_hi:[1,0]
	v_pk_mul_f32 v[24:25], v[158:159], s[36:37] op_sel_hi:[1,0]
	v_pk_mul_f32 v[26:27], v[156:157], s[36:37] op_sel_hi:[1,0]
	v_pk_mul_f32 v[30:31], v[154:155], s[36:37] op_sel_hi:[1,0]
	s_nop 0
	v_lshlrev_b32_e32 v15, 16, v16
	v_and_b32_e32 v16, 0xffff0000, v16
	v_lshlrev_b32_e32 v23, 16, v17
	v_and_b32_e32 v17, 0xffff0000, v17
	v_lshlrev_b32_e32 v28, 16, v18
	v_lshlrev_b32_e32 v32, 16, v19
	v_and_b32_e32 v19, 0xffff0000, v19
	v_fma_f32 v15, v6, v15, v24
	v_fmac_f32_e32 v25, v7, v16
	v_fma_f32 v16, v8, v23, v20
	v_and_b32_e32 v18, 0xffff0000, v18
	v_fmac_f32_e32 v21, v9, v17
	v_fma_f32 v17, v2, v28, v30
	v_fmac_f32_e32 v27, v5, v19
	v_mul_f32_e32 v19, 0x3d372713, v15
	v_mul_f32_e32 v20, 0x3d372713, v25
	v_mul_f32_e32 v23, 0x3d372713, v16
	v_fmac_f32_e32 v31, v3, v18
	v_fma_f32 v18, v4, v32, v26
	v_mul_f32_e32 v24, 0x3d372713, v21
	v_mul_f32_e32 v26, 0x3d372713, v17
	v_mul_f32_e32 v19, v15, v19
	v_mul_f32_e32 v20, v25, v20
	v_mul_f32_e32 v23, v16, v23
	v_mul_f32_e32 v24, v21, v24
	v_mul_f32_e32 v26, v17, v26
	v_fma_f32 v19, v15, v19, v15
	v_fma_f32 v20, v25, v20, v25
	v_fma_f32 v23, v16, v23, v16
	v_fma_f32 v24, v21, v24, v21
	v_fma_f32 v26, v17, v26, v17
	v_mul_f32_e32 v19, 0x3fcc422a, v19
	v_mul_f32_e32 v20, 0x3fcc422a, v20
	v_mul_f32_e32 v23, 0x3fcc422a, v23
	v_mul_f32_e32 v24, 0x3fcc422a, v24
	v_mul_f32_e32 v26, 0x3fcc422a, v26
	v_mul_f32_e32 v19, 0xbfb8aa3b, v19
	v_mul_f32_e32 v20, 0xbfb8aa3b, v20
	v_mul_f32_e32 v23, 0xbfb8aa3b, v23
	v_mul_f32_e32 v24, 0xbfb8aa3b, v24
	v_mul_f32_e32 v26, 0xbfb8aa3b, v26
	v_exp_f32_e32 v19, v19
	v_exp_f32_e32 v20, v20
	v_exp_f32_e32 v23, v23
	v_exp_f32_e32 v24, v24
	v_exp_f32_e32 v26, v26
	v_mul_f32_e32 v28, 0x3d372713, v31
	v_mul_f32_e32 v30, 0x3d372713, v18
	v_mul_f32_e32 v32, 0x3d372713, v27
	v_mul_f32_e32 v28, v31, v28
	v_mul_f32_e32 v30, v18, v30
	v_mul_f32_e32 v32, v27, v32
	v_fma_f32 v28, v31, v28, v31
	v_fma_f32 v30, v18, v30, v18
	v_fma_f32 v32, v27, v32, v27
	v_add_f32_e32 v19, 1.0, v19
	v_add_f32_e32 v20, 1.0, v20
	v_add_f32_e32 v23, 1.0, v23
	v_mul_f32_e32 v28, 0x3fcc422a, v28
	v_mul_f32_e32 v30, 0x3fcc422a, v30
	v_mul_f32_e32 v32, 0x3fcc422a, v32
	v_add_f32_e32 v24, 1.0, v24
	v_add_f32_e32 v26, 1.0, v26
	v_rcp_f32_e32 v19, v19
	v_rcp_f32_e32 v20, v20
	v_rcp_f32_e32 v23, v23
	v_mul_f32_e32 v28, 0xbfb8aa3b, v28
	v_mul_f32_e32 v30, 0xbfb8aa3b, v30
	v_mul_f32_e32 v32, 0xbfb8aa3b, v32
	v_rcp_f32_e32 v24, v24
	v_rcp_f32_e32 v26, v26
	v_exp_f32_e32 v28, v28
	v_exp_f32_e32 v30, v30
	v_exp_f32_e32 v32, v32
	v_mul_f32_e32 v15, v15, v19
	v_mul_f32_e32 v19, v25, v20
	v_mul_f32_e32 v20, v16, v23
	v_mul_f32_e32 v21, v21, v24
	v_mul_f32_e32 v23, v17, v26
	v_cvt_pk_bf16_f32 v16, v15, v19
	v_cvt_pk_bf16_f32 v17, v20, v21
	v_lshl_add_u32 v20, v14, 6, v29
	v_add_f32_e32 v28, 1.0, v28
	v_add_f32_e32 v30, 1.0, v30
	v_add_f32_e32 v32, 1.0, v32
	v_ashrrev_i32_e32 v21, 31, v20
	v_rcp_f32_e32 v28, v28
	v_rcp_f32_e32 v30, v30
	v_rcp_f32_e32 v32, v32
	v_lshlrev_b64 v[20:21], 10, v[20:21]
	v_lshl_add_u64 v[20:21], s[24:25], 0, v[20:21]
	v_lshl_add_u64 v[20:21], s[2:3], 1, v[20:21]
	v_lshl_add_u64 v[20:21], v[20:21], 0, v[170:171]
	v_mul_f32_e32 v24, v31, v28
	v_mul_f32_e32 v25, v18, v30
	v_mul_f32_e32 v26, v27, v32
	v_cvt_pk_bf16_f32 v18, v23, v24
	v_cvt_pk_bf16_f32 v19, v25, v26
	global_store_dwordx4 v[20:21], v[16:19], off
; #define GAS __attribute__((address_space(1)))
; __device__ __forceinline__ float gelu_tanh(float y) { const float a = 1.5957691216f * (y + 0.044715f * y * y * y); return y * sigmoidf_(a); }
; __device__ __forceinline__ unsigned cvt_pk_bf16(float lo, float hi) { unsigned r; asm volatile("v_cvt_pk_bf16_f32 %0, %1, %2" : "=v"(r) : "v"(lo), "v"(hi)); return r; }
;     __device__ __forceinline__ void operator()(const f32x4 (&acc)[2][2][4][2], const Unit& u, int wr, int wc, int fr, int fq) const {
;     ...
;                 for (int m = 0; m < 4; ++m) { const int inst = inst0 + ai * 128 + m * 16;
;                     if (inst < MT / 64) {
;                         const v4u uu = *(const GAS v4u*)(u2 + ((size_t)(g * NINST + inst) * KS2 + cidx));
;                         const f32x4 a0 = acc[ai][bj][m][0] * S5_INV, a1 = acc[ai][bj][m][1] * S5_INV;
;                         const float y0 = a0[0] + d0[0] * bflo(uu.x), y1 = a0[1] + d0[1] * bfhi(uu.x), y2 = a0[2] + d0[2] * bflo(uu.y), y3 = a0[3] + d0[3] * bfhi(uu.y);
;                         const float y4 = a1[0] + d1[0] * bflo(uu.z), y5 = a1[1] + d1[1] * bfhi(uu.z), y6 = a1[2] + d1[2] * bflo(uu.w), y7 = a1[3] + d1[3] * bfhi(uu.w);
;                         v4u w; w.x = pg8::cvt_pk_bf16(gelu_tanh(y0), gelu_tanh(y1)); w.y = pg8::cvt_pk_bf16(gelu_tanh(y2), gelu_tanh(y3));
;                         w.z = pg8::cvt_pk_bf16(gelu_tanh(y4), gelu_tanh(y5)); w.w = pg8::cvt_pk_bf16(gelu_tanh(y6), gelu_tanh(y7));
;                         *(GAS v4u*)(z + ((size_t)(inst * 64 + t) * DSSM + g * 16 + o0)) = w; } } }
.LBB0_544:
	s_or_b64 exec, exec, s[4:5]
	v_or_b32_e32 v15, 16, v14
	v_cmp_gt_i32_e64 s[4:5], s65, v15
	v_add_u32_e32 v23, s20, v15
	s_and_saveexec_b64 s[6:7], s[4:5]
	s_cbranch_execz .LBB0_546
	v_mov_b64_e32 v[16:17], s[22:23]
	v_mad_i64_i32 v[16:17], s[8:9], v23, s66, v[16:17]
	v_lshl_add_u64 v[16:17], v[10:11], 1, v[16:17]
	v_mov_b64_e32 v[16:17], v[200:201]
	v_mov_b64_e32 v[18:19], v[202:203]
	v_pk_mul_f32 v[24:25], v[150:151], s[36:37] op_sel_hi:[1,0]
	v_pk_mul_f32 v[20:21], v[152:153], s[36:37] op_sel_hi:[1,0]
	v_pk_mul_f32 v[26:27], v[148:149], s[36:37] op_sel_hi:[1,0]
	v_pk_mul_f32 v[30:31], v[146:147], s[36:37] op_sel_hi:[1,0]
	s_nop 0
	v_lshlrev_b32_e32 v28, 16, v16
	v_and_b32_e32 v16, 0xffff0000, v16
	v_lshlrev_b32_e32 v32, 16, v17
	v_and_b32_e32 v17, 0xffff0000, v17
	v_fmac_f32_e32 v25, v7, v16
	v_lshlrev_b32_e32 v33, 16, v18
	v_and_b32_e32 v18, 0xffff0000, v18
	v_lshlrev_b32_e32 v180, 16, v19
	v_and_b32_e32 v19, 0xffff0000, v19
	v_fma_f32 v24, v6, v28, v24
	v_fma_f32 v16, v8, v32, v20
	v_fmac_f32_e32 v21, v9, v17
	v_mul_f32_e32 v20, 0x3d372713, v25
	v_fma_f32 v17, v2, v33, v30
	v_fmac_f32_e32 v31, v3, v18
	v_fma_f32 v18, v4, v180, v26
	v_fmac_f32_e32 v27, v5, v19
	v_mul_f32_e32 v19, 0x3d372713, v24
	v_mul_f32_e32 v26, 0x3d372713, v16
	v_mul_f32_e32 v28, 0x3d372713, v21
	v_mul_f32_e32 v20, v25, v20
	v_mul_f32_e32 v30, 0x3d372713, v17
	v_mul_f32_e32 v19, v24, v19
	v_mul_f32_e32 v26, v16, v26
	v_mul_f32_e32 v28, v21, v28
	v_fma_f32 v20, v25, v20, v25
	v_mul_f32_e32 v30, v17, v30
	v_fma_f32 v19, v24, v19, v24
	v_fma_f32 v26, v16, v26, v16
	v_fma_f32 v28, v21, v28, v21
	v_mul_f32_e32 v20, 0x3fcc422a, v20
	v_fma_f32 v30, v17, v30, v17
	v_mul_f32_e32 v19, 0x3fcc422a, v19
	v_mul_f32_e32 v26, 0x3fcc422a, v26
	v_mul_f32_e32 v28, 0x3fcc422a, v28
	v_mul_f32_e32 v20, 0xbfb8aa3b, v20
	v_mul_f32_e32 v30, 0x3fcc422a, v30
	v_mul_f32_e32 v19, 0xbfb8aa3b, v19
	v_mul_f32_e32 v26, 0xbfb8aa3b, v26
	v_mul_f32_e32 v28, 0xbfb8aa3b, v28
	v_exp_f32_e32 v20, v20
	v_mul_f32_e32 v30, 0xbfb8aa3b, v30
	v_exp_f32_e32 v19, v19
	v_exp_f32_e32 v26, v26
	v_exp_f32_e32 v28, v28
	v_mul_f32_e32 v32, 0x3d372713, v31
	v_mul_f32_e32 v33, 0x3d372713, v18
	v_mul_f32_e32 v180, 0x3d372713, v27
	v_exp_f32_e32 v30, v30
	v_mul_f32_e32 v32, v31, v32
	v_mul_f32_e32 v33, v18, v33
	v_mul_f32_e32 v180, v27, v180
	v_fma_f32 v32, v31, v32, v31
	v_fma_f32 v33, v18, v33, v18
	v_fma_f32 v180, v27, v180, v27
	v_add_f32_e32 v20, 1.0, v20
	v_mul_f32_e32 v32, 0x3fcc422a, v32
	v_mul_f32_e32 v33, 0x3fcc422a, v33
	v_mul_f32_e32 v180, 0x3fcc422a, v180
	v_add_f32_e32 v19, 1.0, v19
	v_add_f32_e32 v26, 1.0, v26
	v_add_f32_e32 v28, 1.0, v28
	v_rcp_f32_e32 v20, v20
	v_mul_f32_e32 v32, 0xbfb8aa3b, v32
	v_mul_f32_e32 v33, 0xbfb8aa3b, v33
	v_mul_f32_e32 v180, 0xbfb8aa3b, v180
	v_add_f32_e32 v30, 1.0, v30
	v_rcp_f32_e32 v19, v19
	v_rcp_f32_e32 v26, v26
	v_rcp_f32_e32 v28, v28
	v_exp_f32_e32 v32, v32
	v_exp_f32_e32 v33, v33
	v_exp_f32_e32 v180, v180
	v_rcp_f32_e32 v30, v30
	v_mul_f32_e32 v20, v25, v20
	v_mul_f32_e32 v19, v24, v19
	v_mul_f32_e32 v24, v16, v26
	v_mul_f32_e32 v21, v21, v28
	v_cvt_pk_bf16_f32 v16, v19, v20
	v_lshl_add_u32 v20, v15, 6, v29
	v_add_f32_e32 v32, 1.0, v32
	v_add_f32_e32 v33, 1.0, v33
	v_add_f32_e32 v180, 1.0, v180
	v_mul_f32_e32 v25, v17, v30
	v_cvt_pk_bf16_f32 v17, v24, v21
	v_ashrrev_i32_e32 v21, 31, v20
	v_rcp_f32_e32 v32, v32
	v_rcp_f32_e32 v33, v33
	v_rcp_f32_e32 v180, v180
	v_lshlrev_b64 v[20:21], 10, v[20:21]
	v_lshl_add_u64 v[20:21], s[24:25], 0, v[20:21]
	v_lshl_add_u64 v[20:21], s[2:3], 1, v[20:21]
	v_lshl_add_u64 v[20:21], v[20:21], 0, v[170:171]
	v_mul_f32_e32 v26, v31, v32
	v_mul_f32_e32 v28, v18, v33
	v_mul_f32_e32 v27, v27, v180
	v_cvt_pk_bf16_f32 v18, v25, v26
	v_cvt_pk_bf16_f32 v19, v28, v27
	global_store_dwordx4 v[20:21], v[16:19], off
.LBB0_546:
	s_or_b64 exec, exec, s[6:7]
	s_nop 0
	v_or_b32_e32 v16, 32, v14
	v_cmp_gt_i32_e64 s[6:7], s65, v16
	v_add_u32_e32 v24, s20, v16
	s_and_saveexec_b64 s[8:9], s[6:7]
	s_cbranch_execz .LBB0_548
	v_mov_b64_e32 v[18:19], s[22:23]
	v_mad_i64_i32 v[18:19], s[10:11], v24, s66, v[18:19]
	v_lshl_add_u64 v[18:19], v[10:11], 1, v[18:19]
	v_mov_b64_e32 v[18:19], v[204:205]
	v_mov_b64_e32 v[20:21], v[206:207]
	v_pk_mul_f32 v[26:27], v[144:145], s[36:37] op_sel_hi:[1,0]
	v_pk_mul_f32 v[30:31], v[142:143], s[36:37] op_sel_hi:[1,0]
	v_pk_mul_f32 v[32:33], v[140:141], s[36:37] op_sel_hi:[1,0]
	v_pk_mul_f32 v[180:181], v[138:139], s[36:37] op_sel_hi:[1,0]
	s_nop 0
	v_lshlrev_b32_e32 v17, 16, v18
	v_and_b32_e32 v18, 0xffff0000, v18
	v_lshlrev_b32_e32 v25, 16, v19
	v_and_b32_e32 v19, 0xffff0000, v19
	v_lshlrev_b32_e32 v28, 16, v20
	v_lshlrev_b32_e32 v182, 16, v21
	v_and_b32_e32 v21, 0xffff0000, v21
	v_fma_f32 v17, v6, v17, v30
	v_fmac_f32_e32 v31, v7, v18
	v_fma_f32 v18, v8, v25, v26
	v_fmac_f32_e32 v27, v9, v19
	v_and_b32_e32 v20, 0xffff0000, v20
	v_fma_f32 v19, v2, v28, v180
	v_fmac_f32_e32 v33, v5, v21
	v_mul_f32_e32 v21, 0x3d372713, v17
	v_mul_f32_e32 v25, 0x3d372713, v31
	v_mul_f32_e32 v26, 0x3d372713, v18
	v_mul_f32_e32 v28, 0x3d372713, v27
	v_fmac_f32_e32 v181, v3, v20
	v_fma_f32 v20, v4, v182, v32
	v_mul_f32_e32 v30, 0x3d372713, v19
	v_mul_f32_e32 v21, v17, v21
	v_mul_f32_e32 v25, v31, v25
	v_mul_f32_e32 v26, v18, v26
	v_mul_f32_e32 v28, v27, v28
	v_mul_f32_e32 v32, 0x3d372713, v181
	v_mul_f32_e32 v180, 0x3d372713, v20
	v_mul_f32_e32 v30, v19, v30
	v_fma_f32 v21, v17, v21, v17
	v_fma_f32 v25, v31, v25, v31
	v_fma_f32 v26, v18, v26, v18
	v_fma_f32 v28, v27, v28, v27
	v_mul_f32_e32 v32, v181, v32
	v_mul_f32_e32 v180, v20, v180
	v_fma_f32 v30, v19, v30, v19
	v_mul_f32_e32 v21, 0x3fcc422a, v21
	v_mul_f32_e32 v25, 0x3fcc422a, v25
; #define GAS __attribute__((address_space(1)))
; __device__ __forceinline__ float gelu_tanh(float y) { const float a = 1.5957691216f * (y + 0.044715f * y * y * y); return y * sigmoidf_(a); }
; __device__ __forceinline__ unsigned cvt_pk_bf16(float lo, float hi) { unsigned r; asm volatile("v_cvt_pk_bf16_f32 %0, %1, %2" : "=v"(r) : "v"(lo), "v"(hi)); return r; }
;     __device__ __forceinline__ void operator()(const f32x4 (&acc)[2][2][4][2], const Unit& u, int wr, int wc, int fr, int fq) const {
;     ...
;                 for (int m = 0; m < 4; ++m) { const int inst = inst0 + ai * 128 + m * 16;
;                     if (inst < MT / 64) {
;                         const v4u uu = *(const GAS v4u*)(u2 + ((size_t)(g * NINST + inst) * KS2 + cidx));
;                         const f32x4 a0 = acc[ai][bj][m][0] * S5_INV, a1 = acc[ai][bj][m][1] * S5_INV;
;                         const float y0 = a0[0] + d0[0] * bflo(uu.x), y1 = a0[1] + d0[1] * bfhi(uu.x), y2 = a0[2] + d0[2] * bflo(uu.y), y3 = a0[3] + d0[3] * bfhi(uu.y);
;                         const float y4 = a1[0] + d1[0] * bflo(uu.z), y5 = a1[1] + d1[1] * bfhi(uu.z), y6 = a1[2] + d1[2] * bflo(uu.w), y7 = a1[3] + d1[3] * bfhi(uu.w);
;                         v4u w; w.x = pg8::cvt_pk_bf16(gelu_tanh(y0), gelu_tanh(y1)); w.y = pg8::cvt_pk_bf16(gelu_tanh(y2), gelu_tanh(y3));
;                         w.z = pg8::cvt_pk_bf16(gelu_tanh(y4), gelu_tanh(y5)); w.w = pg8::cvt_pk_bf16(gelu_tanh(y6), gelu_tanh(y7));
;                         *(GAS v4u*)(z + ((size_t)(inst * 64 + t) * DSSM + g * 16 + o0)) = w; } } }
	v_mul_f32_e32 v26, 0x3fcc422a, v26
	v_mul_f32_e32 v28, 0x3fcc422a, v28
	v_fma_f32 v32, v181, v32, v181
	v_fma_f32 v180, v20, v180, v20
	v_mul_f32_e32 v30, 0x3fcc422a, v30
	v_mul_f32_e32 v21, 0xbfb8aa3b, v21
	v_mul_f32_e32 v25, 0xbfb8aa3b, v25
	v_mul_f32_e32 v26, 0xbfb8aa3b, v26
	v_mul_f32_e32 v28, 0xbfb8aa3b, v28
	v_mul_f32_e32 v32, 0x3fcc422a, v32
	v_mul_f32_e32 v180, 0x3fcc422a, v180
	v_mul_f32_e32 v30, 0xbfb8aa3b, v30
	v_exp_f32_e32 v21, v21
	v_exp_f32_e32 v25, v25
	v_exp_f32_e32 v26, v26
	v_exp_f32_e32 v28, v28
	v_mul_f32_e32 v32, 0xbfb8aa3b, v32
	v_mul_f32_e32 v180, 0xbfb8aa3b, v180
	v_exp_f32_e32 v30, v30
	v_mul_f32_e32 v182, 0x3d372713, v33
	v_exp_f32_e32 v32, v32
	v_exp_f32_e32 v180, v180
	v_mul_f32_e32 v182, v33, v182
	v_fma_f32 v182, v33, v182, v33
	v_add_f32_e32 v21, 1.0, v21
	v_add_f32_e32 v25, 1.0, v25
	v_add_f32_e32 v26, 1.0, v26
	v_add_f32_e32 v28, 1.0, v28
	v_mul_f32_e32 v182, 0x3fcc422a, v182
	v_add_f32_e32 v30, 1.0, v30
	v_rcp_f32_e32 v21, v21
	v_rcp_f32_e32 v25, v25
	v_rcp_f32_e32 v26, v26
	v_rcp_f32_e32 v28, v28
	v_mul_f32_e32 v182, 0xbfb8aa3b, v182
	v_add_f32_e32 v32, 1.0, v32
	v_add_f32_e32 v180, 1.0, v180
	v_rcp_f32_e32 v30, v30
	v_exp_f32_e32 v182, v182
	v_rcp_f32_e32 v32, v32
	v_rcp_f32_e32 v180, v180
	v_mul_f32_e32 v17, v17, v21
	v_mul_f32_e32 v21, v31, v25
	v_mul_f32_e32 v25, v18, v26
	v_mul_f32_e32 v26, v27, v28
	v_mul_f32_e32 v27, v19, v30
	v_cvt_pk_bf16_f32 v18, v17, v21
	v_cvt_pk_bf16_f32 v19, v25, v26
	v_lshl_add_u32 v26, v16, 6, v29
	v_add_f32_e32 v182, 1.0, v182
	v_mul_f32_e32 v28, v181, v32
	v_mul_f32_e32 v30, v20, v180
	v_cvt_pk_bf16_f32 v20, v27, v28
	v_ashrrev_i32_e32 v27, 31, v26
	v_rcp_f32_e32 v182, v182
	v_lshlrev_b64 v[26:27], 10, v[26:27]
	v_lshl_add_u64 v[26:27], s[24:25], 0, v[26:27]
	v_lshl_add_u64 v[26:27], s[2:3], 1, v[26:27]
	v_lshl_add_u64 v[26:27], v[26:27], 0, v[170:171]
	v_mul_f32_e32 v31, v33, v182
	v_cvt_pk_bf16_f32 v21, v30, v31
	global_store_dwordx4 v[26:27], v[18:21], off
.LBB0_548:
	s_or_b64 exec, exec, s[8:9]
	v_or_b32_e32 v17, 48, v14
	v_cmp_gt_i32_e64 s[8:9], s65, v17
	v_add_u32_e32 v25, s20, v17
	s_and_saveexec_b64 s[10:11], s[8:9]
	s_cbranch_execz .LBB0_550
	v_mov_b64_e32 v[18:19], s[22:23]
	v_mad_i64_i32 v[18:19], s[12:13], v25, s66, v[18:19]
	v_lshl_add_u64 v[18:19], v[10:11], 1, v[18:19]
	v_mov_b64_e32 v[18:19], v[208:209]
	v_mov_b64_e32 v[20:21], v[210:211]
	v_pk_mul_f32 v[30:31], v[134:135], s[36:37] op_sel_hi:[1,0]
	v_pk_mul_f32 v[26:27], v[136:137], s[36:37] op_sel_hi:[1,0]
	v_pk_mul_f32 v[32:33], v[132:133], s[36:37] op_sel_hi:[1,0]
	v_pk_mul_f32 v[180:181], v[130:131], s[36:37] op_sel_hi:[1,0]
	s_nop 0
	v_lshlrev_b32_e32 v28, 16, v18
	v_and_b32_e32 v18, 0xffff0000, v18
	v_lshlrev_b32_e32 v182, 16, v19
	v_and_b32_e32 v19, 0xffff0000, v19
	v_fmac_f32_e32 v31, v7, v18
	v_lshlrev_b32_e32 v183, 16, v20
	v_and_b32_e32 v20, 0xffff0000, v20
	v_lshlrev_b32_e32 v184, 16, v21
	v_and_b32_e32 v21, 0xffff0000, v21
	v_fma_f32 v28, v6, v28, v30
	v_fma_f32 v18, v8, v182, v26
	v_fmac_f32_e32 v27, v9, v19
	v_mul_f32_e32 v26, 0x3d372713, v31
	v_fma_f32 v19, v2, v183, v180
	v_fmac_f32_e32 v181, v3, v20
	v_fma_f32 v20, v4, v184, v32
	v_fmac_f32_e32 v33, v5, v21
	v_mul_f32_e32 v21, 0x3d372713, v28
	v_mul_f32_e32 v30, 0x3d372713, v18
	v_mul_f32_e32 v32, 0x3d372713, v27
	v_mul_f32_e32 v26, v31, v26
	v_mul_f32_e32 v180, 0x3d372713, v19
	v_mul_f32_e32 v21, v28, v21
	v_mul_f32_e32 v30, v18, v30
	v_mul_f32_e32 v32, v27, v32
	v_fma_f32 v26, v31, v26, v31
	v_mul_f32_e32 v180, v19, v180
	v_fma_f32 v21, v28, v21, v28
	v_fma_f32 v30, v18, v30, v18
	v_fma_f32 v32, v27, v32, v27
	v_mul_f32_e32 v26, 0x3fcc422a, v26
	v_fma_f32 v180, v19, v180, v19
	v_mul_f32_e32 v21, 0x3fcc422a, v21
	v_mul_f32_e32 v30, 0x3fcc422a, v30
	v_mul_f32_e32 v32, 0x3fcc422a, v32
	v_mul_f32_e32 v26, 0xbfb8aa3b, v26
	v_mul_f32_e32 v180, 0x3fcc422a, v180
	v_mul_f32_e32 v21, 0xbfb8aa3b, v21
	v_mul_f32_e32 v30, 0xbfb8aa3b, v30
	v_mul_f32_e32 v32, 0xbfb8aa3b, v32
	v_exp_f32_e32 v26, v26
	v_mul_f32_e32 v180, 0xbfb8aa3b, v180
	v_exp_f32_e32 v21, v21
	v_exp_f32_e32 v30, v30
	v_exp_f32_e32 v32, v32
	v_mul_f32_e32 v182, 0x3d372713, v181
	v_mul_f32_e32 v183, 0x3d372713, v20
	v_mul_f32_e32 v184, 0x3d372713, v33
	v_exp_f32_e32 v180, v180
	v_mul_f32_e32 v182, v181, v182
	v_mul_f32_e32 v183, v20, v183
	v_mul_f32_e32 v184, v33, v184
	v_fma_f32 v182, v181, v182, v181
	v_fma_f32 v183, v20, v183, v20
	v_fma_f32 v184, v33, v184, v33
	v_add_f32_e32 v26, 1.0, v26
	v_mul_f32_e32 v182, 0x3fcc422a, v182
	v_mul_f32_e32 v183, 0x3fcc422a, v183
	v_mul_f32_e32 v184, 0x3fcc422a, v184
	v_add_f32_e32 v21, 1.0, v21
	v_add_f32_e32 v30, 1.0, v30
	v_add_f32_e32 v32, 1.0, v32
	v_rcp_f32_e32 v26, v26
	v_mul_f32_e32 v182, 0xbfb8aa3b, v182
	v_mul_f32_e32 v183, 0xbfb8aa3b, v183
	v_mul_f32_e32 v184, 0xbfb8aa3b, v184
	v_add_f32_e32 v180, 1.0, v180
	v_rcp_f32_e32 v21, v21
	v_rcp_f32_e32 v30, v30
	v_rcp_f32_e32 v32, v32
	v_exp_f32_e32 v182, v182
	v_exp_f32_e32 v183, v183
	v_exp_f32_e32 v184, v184
	v_rcp_f32_e32 v180, v180
	v_mul_f32_e32 v26, v31, v26
	v_mul_f32_e32 v21, v28, v21
	v_mul_f32_e32 v28, v18, v30
	v_mul_f32_e32 v27, v27, v32
	v_cvt_pk_bf16_f32 v18, v21, v26
	v_lshl_add_u32 v26, v17, 6, v29
	v_add_f32_e32 v182, 1.0, v182
	v_add_f32_e32 v183, 1.0, v183
	v_add_f32_e32 v184, 1.0, v184
	v_mul_f32_e32 v30, v19, v180
	v_cvt_pk_bf16_f32 v19, v28, v27
	v_ashrrev_i32_e32 v27, 31, v26
	v_rcp_f32_e32 v182, v182
	v_rcp_f32_e32 v183, v183
	v_rcp_f32_e32 v184, v184
	v_lshlrev_b64 v[26:27], 10, v[26:27]
	v_lshl_add_u64 v[26:27], s[24:25], 0, v[26:27]
	v_lshl_add_u64 v[26:27], s[2:3], 1, v[26:27]
	v_lshl_add_u64 v[26:27], v[26:27], 0, v[170:171]
	v_mul_f32_e32 v31, v181, v182
	v_mul_f32_e32 v32, v20, v183
	v_mul_f32_e32 v33, v33, v184
	v_cvt_pk_bf16_f32 v20, v30, v31
	v_cvt_pk_bf16_f32 v21, v32, v33
	global_store_dwordx4 v[26:27], v[18:21], off
; #define GAS __attribute__((address_space(1)))
; __device__ __forceinline__ float gelu_tanh(float y) { const float a = 1.5957691216f * (y + 0.044715f * y * y * y); return y * sigmoidf_(a); }
; __device__ __forceinline__ unsigned cvt_pk_bf16(float lo, float hi) { unsigned r; asm volatile("v_cvt_pk_bf16_f32 %0, %1, %2" : "=v"(r) : "v"(lo), "v"(hi)); return r; }
;     __device__ __forceinline__ void operator()(const f32x4 (&acc)[2][2][4][2], const Unit& u, int wr, int wc, int fr, int fq) const {
;     ...
;                 for (int m = 0; m < 4; ++m) { const int inst = inst0 + ai * 128 + m * 16;
;                     if (inst < MT / 64) {
;                         const v4u uu = *(const GAS v4u*)(u2 + ((size_t)(g * NINST + inst) * KS2 + cidx));
;                         const f32x4 a0 = acc[ai][bj][m][0] * S5_INV, a1 = acc[ai][bj][m][1] * S5_INV;
;                         const float y0 = a0[0] + d0[0] * bflo(uu.x), y1 = a0[1] + d0[1] * bfhi(uu.x), y2 = a0[2] + d0[2] * bflo(uu.y), y3 = a0[3] + d0[3] * bfhi(uu.y);
;                         const float y4 = a1[0] + d1[0] * bflo(uu.z), y5 = a1[1] + d1[1] * bfhi(uu.z), y6 = a1[2] + d1[2] * bflo(uu.w), y7 = a1[3] + d1[3] * bfhi(uu.w);
;                         v4u w; w.x = pg8::cvt_pk_bf16(gelu_tanh(y0), gelu_tanh(y1)); w.y = pg8::cvt_pk_bf16(gelu_tanh(y2), gelu_tanh(y3));
;                         w.z = pg8::cvt_pk_bf16(gelu_tanh(y4), gelu_tanh(y5)); w.w = pg8::cvt_pk_bf16(gelu_tanh(y6), gelu_tanh(y7));
;                         *(GAS v4u*)(z + ((size_t)(inst * 64 + t) * DSSM + g * 16 + o0)) = w; } } }
.LBB0_550:
	s_or_b64 exec, exec, s[10:11]
	s_nop 0
	v_add_u32_e32 v18, 0x80, v14
	v_cmp_gt_i32_e64 s[10:11], s68, v14
	v_add_u32_e32 v26, s20, v18
	s_and_saveexec_b64 s[12:13], s[10:11]
	s_cbranch_execz .LBB0_552
	v_mov_b64_e32 v[20:21], s[22:23]
	v_mad_i64_i32 v[20:21], s[14:15], v26, s66, v[20:21]
	v_lshl_add_u64 v[20:21], v[10:11], 1, v[20:21]
	v_mov_b64_e32 v[30:31], v[212:213]
	v_mov_b64_e32 v[32:33], v[214:215]
	v_pk_mul_f32 v[20:21], v[96:97], s[36:37] op_sel_hi:[1,0]
	v_pk_mul_f32 v[180:181], v[94:95], s[36:37] op_sel_hi:[1,0]
	v_pk_mul_f32 v[184:185], v[90:91], s[36:37] op_sel_hi:[1,0]
	v_pk_mul_f32 v[182:183], v[92:93], s[36:37] op_sel_hi:[1,0]
	s_nop 0
	v_lshlrev_b32_e32 v19, 16, v30
	v_and_b32_e32 v27, 0xffff0000, v30
	v_lshlrev_b32_e32 v28, 16, v31
	v_and_b32_e32 v30, 0xffff0000, v31
	v_lshlrev_b32_e32 v31, 16, v32
	v_and_b32_e32 v32, 0xffff0000, v32
	v_fma_f32 v19, v6, v19, v180
	v_fmac_f32_e32 v181, v7, v27
	v_fma_f32 v20, v8, v28, v20
	v_lshlrev_b32_e32 v186, 16, v33
	v_and_b32_e32 v33, 0xffff0000, v33
	v_fmac_f32_e32 v21, v9, v30
	v_fma_f32 v27, v2, v31, v184
	v_fmac_f32_e32 v185, v3, v32
	v_mul_f32_e32 v30, 0x3d372713, v19
	v_mul_f32_e32 v31, 0x3d372713, v181
	v_mul_f32_e32 v32, 0x3d372713, v20
	v_fmac_f32_e32 v183, v5, v33
	v_mul_f32_e32 v33, 0x3d372713, v21
	v_mul_f32_e32 v30, v19, v30
	v_mul_f32_e32 v31, v181, v31
	v_mul_f32_e32 v32, v20, v32
	v_mul_f32_e32 v33, v21, v33
	v_fma_f32 v30, v19, v30, v19
	v_fma_f32 v31, v181, v31, v181
	v_fma_f32 v32, v20, v32, v20
	v_fma_f32 v33, v21, v33, v21
	v_mul_f32_e32 v30, 0x3fcc422a, v30
	v_mul_f32_e32 v31, 0x3fcc422a, v31
	v_mul_f32_e32 v32, 0x3fcc422a, v32
	v_mul_f32_e32 v33, 0x3fcc422a, v33
	v_mul_f32_e32 v30, 0xbfb8aa3b, v30
	v_mul_f32_e32 v31, 0xbfb8aa3b, v31
	v_mul_f32_e32 v32, 0xbfb8aa3b, v32
	v_mul_f32_e32 v33, 0xbfb8aa3b, v33
	v_exp_f32_e32 v30, v30
	v_exp_f32_e32 v31, v31
	v_exp_f32_e32 v32, v32
	v_fma_f32 v28, v4, v186, v182
	v_mul_f32_e32 v182, 0x3d372713, v185
	v_mul_f32_e32 v186, 0x3d372713, v183
	v_exp_f32_e32 v33, v33
	v_mul_f32_e32 v180, 0x3d372713, v27
	v_mul_f32_e32 v184, 0x3d372713, v28
	v_mul_f32_e32 v182, v185, v182
	v_mul_f32_e32 v186, v183, v186
	v_mul_f32_e32 v180, v27, v180
	v_mul_f32_e32 v184, v28, v184
	v_fma_f32 v182, v185, v182, v185
	v_fma_f32 v186, v183, v186, v183
	v_fma_f32 v180, v27, v180, v27
	v_fma_f32 v184, v28, v184, v28
	v_mul_f32_e32 v182, 0x3fcc422a, v182
	v_mul_f32_e32 v186, 0x3fcc422a, v186
	v_add_f32_e32 v30, 1.0, v30
	v_add_f32_e32 v31, 1.0, v31
	v_add_f32_e32 v32, 1.0, v32
	v_mul_f32_e32 v180, 0x3fcc422a, v180
	v_mul_f32_e32 v184, 0x3fcc422a, v184
	v_mul_f32_e32 v182, 0xbfb8aa3b, v182
	v_mul_f32_e32 v186, 0xbfb8aa3b, v186
	v_add_f32_e32 v33, 1.0, v33
	v_rcp_f32_e32 v30, v30
	v_rcp_f32_e32 v31, v31
	v_rcp_f32_e32 v32, v32
	v_mul_f32_e32 v180, 0xbfb8aa3b, v180
	v_mul_f32_e32 v184, 0xbfb8aa3b, v184
	v_exp_f32_e32 v182, v182
	v_exp_f32_e32 v186, v186
	v_rcp_f32_e32 v33, v33
	v_exp_f32_e32 v180, v180
	v_exp_f32_e32 v184, v184
	v_mul_f32_e32 v19, v19, v30
	v_mul_f32_e32 v30, v181, v31
	v_mul_f32_e32 v20, v20, v32
	v_add_f32_e32 v182, 1.0, v182
	v_add_f32_e32 v186, 1.0, v186
	v_mul_f32_e32 v21, v21, v33
	v_cvt_pk_bf16_f32 v30, v19, v30
	v_cvt_pk_bf16_f32 v31, v20, v21
	v_lshl_add_u32 v20, v18, 6, v29
	v_add_f32_e32 v180, 1.0, v180
	v_add_f32_e32 v184, 1.0, v184
	v_rcp_f32_e32 v182, v182
	v_rcp_f32_e32 v186, v186
	v_ashrrev_i32_e32 v21, 31, v20
	v_rcp_f32_e32 v180, v180
	v_rcp_f32_e32 v184, v184
	v_lshlrev_b64 v[20:21], 10, v[20:21]
	v_lshl_add_u64 v[20:21], s[24:25], 0, v[20:21]
	v_lshl_add_u64 v[20:21], s[2:3], 1, v[20:21]
	v_mul_f32_e32 v32, v185, v182
	v_mul_f32_e32 v33, v183, v186
	v_lshl_add_u64 v[20:21], v[20:21], 0, v[170:171]
	v_mul_f32_e32 v27, v27, v180
	v_mul_f32_e32 v28, v28, v184
	v_cvt_pk_bf16_f32 v32, v27, v32
	v_cvt_pk_bf16_f32 v33, v28, v33
	global_store_dwordx4 v[20:21], v[30:33], off
.LBB0_552:
	s_or_b64 exec, exec, s[12:13]
	v_add_u32_e32 v19, 0x90, v14
	v_cmp_gt_i32_e64 s[12:13], s69, v14
	v_add_u32_e32 v27, s20, v19
	s_and_saveexec_b64 s[14:15], s[12:13]
	s_cbranch_execz .LBB0_554
	v_mov_b64_e32 v[20:21], s[22:23]
	v_mad_i64_i32 v[20:21], s[16:17], v27, s66, v[20:21]
	v_lshl_add_u64 v[20:21], v[10:11], 1, v[20:21]
	v_mov_b64_e32 v[30:31], v[216:217]
	v_mov_b64_e32 v[32:33], v[218:219]
	v_pk_mul_f32 v[20:21], v[88:89], s[36:37] op_sel_hi:[1,0]
	v_pk_mul_f32 v[180:181], v[86:87], s[36:37] op_sel_hi:[1,0]
	v_pk_mul_f32 v[182:183], v[84:85], s[36:37] op_sel_hi:[1,0]
	v_pk_mul_f32 v[184:185], v[82:83], s[36:37] op_sel_hi:[1,0]
	s_nop 0
	v_lshlrev_b32_e32 v186, 16, v31
	v_lshlrev_b32_e32 v28, 16, v30
	v_and_b32_e32 v30, 0xffff0000, v30
	v_and_b32_e32 v31, 0xffff0000, v31
	v_lshlrev_b32_e32 v187, 16, v32
	v_lshlrev_b32_e32 v190, 16, v33
	v_fma_f32 v20, v8, v186, v20
	v_and_b32_e32 v32, 0xffff0000, v32
	v_and_b32_e32 v33, 0xffff0000, v33
	v_fma_f32 v28, v6, v28, v180
	v_fmac_f32_e32 v181, v7, v30
	v_fmac_f32_e32 v21, v9, v31
	v_fma_f32 v30, v2, v187, v184
	v_fma_f32 v31, v4, v190, v182
	v_mul_f32_e32 v180, 0x3d372713, v20
	v_fmac_f32_e32 v185, v3, v32
	v_fmac_f32_e32 v183, v5, v33
	v_mul_f32_e32 v32, 0x3d372713, v28
	v_mul_f32_e32 v33, 0x3d372713, v181
	v_mul_f32_e32 v182, 0x3d372713, v21
	v_mul_f32_e32 v184, 0x3d372713, v30
	v_mul_f32_e32 v187, 0x3d372713, v31
	v_mul_f32_e32 v180, v20, v180
	v_mul_f32_e32 v32, v28, v32
	v_mul_f32_e32 v33, v181, v33
	v_mul_f32_e32 v182, v21, v182
	v_mul_f32_e32 v184, v30, v184
	v_mul_f32_e32 v187, v31, v187
	v_fma_f32 v180, v20, v180, v20
	v_fma_f32 v32, v28, v32, v28
	v_fma_f32 v33, v181, v33, v181
	v_fma_f32 v182, v21, v182, v21
	v_fma_f32 v184, v30, v184, v30
	v_fma_f32 v187, v31, v187, v31
; #define GAS __attribute__((address_space(1)))
; __device__ __forceinline__ float gelu_tanh(float y) { const float a = 1.5957691216f * (y + 0.044715f * y * y * y); return y * sigmoidf_(a); }
; __device__ __forceinline__ unsigned cvt_pk_bf16(float lo, float hi) { unsigned r; asm volatile("v_cvt_pk_bf16_f32 %0, %1, %2" : "=v"(r) : "v"(lo), "v"(hi)); return r; }
;     __device__ __forceinline__ void operator()(const f32x4 (&acc)[2][2][4][2], const Unit& u, int wr, int wc, int fr, int fq) const {
;     ...
;                 for (int m = 0; m < 4; ++m) { const int inst = inst0 + ai * 128 + m * 16;
;                     if (inst < MT / 64) {
;                         const v4u uu = *(const GAS v4u*)(u2 + ((size_t)(g * NINST + inst) * KS2 + cidx));
;                         const f32x4 a0 = acc[ai][bj][m][0] * S5_INV, a1 = acc[ai][bj][m][1] * S5_INV;
;                         const float y0 = a0[0] + d0[0] * bflo(uu.x), y1 = a0[1] + d0[1] * bfhi(uu.x), y2 = a0[2] + d0[2] * bflo(uu.y), y3 = a0[3] + d0[3] * bfhi(uu.y);
;                         const float y4 = a1[0] + d1[0] * bflo(uu.z), y5 = a1[1] + d1[1] * bfhi(uu.z), y6 = a1[2] + d1[2] * bflo(uu.w), y7 = a1[3] + d1[3] * bfhi(uu.w);
;                         v4u w; w.x = pg8::cvt_pk_bf16(gelu_tanh(y0), gelu_tanh(y1)); w.y = pg8::cvt_pk_bf16(gelu_tanh(y2), gelu_tanh(y3));
;                         w.z = pg8::cvt_pk_bf16(gelu_tanh(y4), gelu_tanh(y5)); w.w = pg8::cvt_pk_bf16(gelu_tanh(y6), gelu_tanh(y7));
;                         *(GAS v4u*)(z + ((size_t)(inst * 64 + t) * DSSM + g * 16 + o0)) = w; } } }
	v_mul_f32_e32 v180, 0x3fcc422a, v180
	v_mul_f32_e32 v32, 0x3fcc422a, v32
	v_mul_f32_e32 v33, 0x3fcc422a, v33
	v_mul_f32_e32 v182, 0x3fcc422a, v182
	v_mul_f32_e32 v184, 0x3fcc422a, v184
	v_mul_f32_e32 v187, 0x3fcc422a, v187
	v_mul_f32_e32 v180, 0xbfb8aa3b, v180
	v_mul_f32_e32 v32, 0xbfb8aa3b, v32
	v_mul_f32_e32 v33, 0xbfb8aa3b, v33
	v_mul_f32_e32 v182, 0xbfb8aa3b, v182
	v_mul_f32_e32 v184, 0xbfb8aa3b, v184
	v_mul_f32_e32 v187, 0xbfb8aa3b, v187
	v_exp_f32_e32 v180, v180
	v_exp_f32_e32 v32, v32
	v_exp_f32_e32 v33, v33
	v_exp_f32_e32 v182, v182
	v_exp_f32_e32 v184, v184
	v_exp_f32_e32 v187, v187
	v_mul_f32_e32 v186, 0x3d372713, v185
	v_mul_f32_e32 v190, 0x3d372713, v183
	v_mul_f32_e32 v186, v185, v186
	v_mul_f32_e32 v190, v183, v190
	v_fma_f32 v186, v185, v186, v185
	v_fma_f32 v190, v183, v190, v183
	v_add_f32_e32 v180, 1.0, v180
	v_mul_f32_e32 v186, 0x3fcc422a, v186
	v_mul_f32_e32 v190, 0x3fcc422a, v190
	v_add_f32_e32 v32, 1.0, v32
	v_add_f32_e32 v33, 1.0, v33
	v_add_f32_e32 v182, 1.0, v182
	v_add_f32_e32 v184, 1.0, v184
	v_add_f32_e32 v187, 1.0, v187
	v_rcp_f32_e32 v180, v180
	v_mul_f32_e32 v186, 0xbfb8aa3b, v186
	v_mul_f32_e32 v190, 0xbfb8aa3b, v190
	v_rcp_f32_e32 v32, v32
	v_rcp_f32_e32 v33, v33
	v_rcp_f32_e32 v182, v182
	v_rcp_f32_e32 v184, v184
	v_rcp_f32_e32 v187, v187
	v_exp_f32_e32 v186, v186
	v_exp_f32_e32 v190, v190
	v_mul_f32_e32 v20, v20, v180
	v_mul_f32_e32 v28, v28, v32
	v_mul_f32_e32 v32, v181, v33
	v_mul_f32_e32 v21, v21, v182
	v_mul_f32_e32 v33, v30, v184
	v_mul_f32_e32 v181, v31, v187
	v_cvt_pk_bf16_f32 v30, v28, v32
	v_cvt_pk_bf16_f32 v31, v20, v21
	v_lshl_add_u32 v20, v19, 6, v29
	v_add_f32_e32 v186, 1.0, v186
	v_add_f32_e32 v190, 1.0, v190
	v_ashrrev_i32_e32 v21, 31, v20
	v_rcp_f32_e32 v186, v186
	v_rcp_f32_e32 v190, v190
	v_lshlrev_b64 v[20:21], 10, v[20:21]
	v_lshl_add_u64 v[20:21], s[24:25], 0, v[20:21]
	v_lshl_add_u64 v[20:21], s[2:3], 1, v[20:21]
	v_lshl_add_u64 v[20:21], v[20:21], 0, v[170:171]
	v_mul_f32_e32 v180, v185, v186
	v_mul_f32_e32 v182, v183, v190
	v_cvt_pk_bf16_f32 v32, v33, v180
	v_cvt_pk_bf16_f32 v33, v181, v182
	global_store_dwordx4 v[20:21], v[30:33], off
.LBB0_554:
	s_or_b64 exec, exec, s[14:15]
	v_add_u32_e32 v20, 0xa0, v14
	v_cmp_gt_i32_e64 s[14:15], s67, v14
	v_add_u32_e32 v28, s20, v20
	s_and_saveexec_b64 s[16:17], s[14:15]
	s_cbranch_execz .LBB0_556
	v_mov_b64_e32 v[30:31], s[22:23]
	v_mad_i64_i32 v[30:31], s[74:75], v28, s66, v[30:31]
	v_lshl_add_u64 v[30:31], v[10:11], 1, v[30:31]
	v_mov_b64_e32 v[30:31], v[220:221]
	v_mov_b64_e32 v[32:33], v[222:223]
	v_pk_mul_f32 v[180:181], v[80:81], s[36:37] op_sel_hi:[1,0]
	v_pk_mul_f32 v[182:183], v[78:79], s[36:37] op_sel_hi:[1,0]
	v_pk_mul_f32 v[184:185], v[76:77], s[36:37] op_sel_hi:[1,0]
	v_pk_mul_f32 v[186:187], v[74:75], s[36:37] op_sel_hi:[1,0]
	s_nop 0
	v_lshlrev_b32_e32 v21, 16, v30
	v_and_b32_e32 v30, 0xffff0000, v30
	v_lshlrev_b32_e32 v190, 16, v31
	v_and_b32_e32 v31, 0xffff0000, v31
	v_lshlrev_b32_e32 v191, 16, v32
	v_lshlrev_b32_e32 v192, 16, v33
	v_and_b32_e32 v33, 0xffff0000, v33
	v_fma_f32 v21, v6, v21, v182
	v_fmac_f32_e32 v183, v7, v30
	v_fma_f32 v30, v8, v190, v180
	v_and_b32_e32 v32, 0xffff0000, v32
	v_fmac_f32_e32 v181, v9, v31
	v_fma_f32 v31, v2, v191, v186
	v_fmac_f32_e32 v185, v5, v33
	v_mul_f32_e32 v33, 0x3d372713, v21
	v_mul_f32_e32 v180, 0x3d372713, v183
	v_mul_f32_e32 v182, 0x3d372713, v30
	v_fmac_f32_e32 v187, v3, v32
	v_fma_f32 v32, v4, v192, v184
	v_mul_f32_e32 v184, 0x3d372713, v181
	v_mul_f32_e32 v186, 0x3d372713, v31
	v_mul_f32_e32 v33, v21, v33
	v_mul_f32_e32 v180, v183, v180
	v_mul_f32_e32 v182, v30, v182
	v_mul_f32_e32 v184, v181, v184
	v_mul_f32_e32 v186, v31, v186
	v_fma_f32 v33, v21, v33, v21
	v_fma_f32 v180, v183, v180, v183
	v_fma_f32 v182, v30, v182, v30
	v_fma_f32 v184, v181, v184, v181
	v_fma_f32 v186, v31, v186, v31
	v_mul_f32_e32 v33, 0x3fcc422a, v33
	v_mul_f32_e32 v180, 0x3fcc422a, v180
	v_mul_f32_e32 v182, 0x3fcc422a, v182
	v_mul_f32_e32 v184, 0x3fcc422a, v184
	v_mul_f32_e32 v186, 0x3fcc422a, v186
	v_mul_f32_e32 v33, 0xbfb8aa3b, v33
	v_mul_f32_e32 v180, 0xbfb8aa3b, v180
	v_mul_f32_e32 v182, 0xbfb8aa3b, v182
	v_mul_f32_e32 v184, 0xbfb8aa3b, v184
	v_mul_f32_e32 v186, 0xbfb8aa3b, v186
	v_exp_f32_e32 v33, v33
	v_exp_f32_e32 v180, v180
	v_exp_f32_e32 v182, v182
	v_exp_f32_e32 v184, v184
	v_exp_f32_e32 v186, v186
	v_mul_f32_e32 v190, 0x3d372713, v187
	v_mul_f32_e32 v191, 0x3d372713, v32
	v_mul_f32_e32 v192, 0x3d372713, v185
	v_mul_f32_e32 v190, v187, v190
	v_mul_f32_e32 v191, v32, v191
	v_mul_f32_e32 v192, v185, v192
	v_fma_f32 v190, v187, v190, v187
	v_fma_f32 v191, v32, v191, v32
	v_fma_f32 v192, v185, v192, v185
	v_add_f32_e32 v33, 1.0, v33
	v_add_f32_e32 v180, 1.0, v180
	v_add_f32_e32 v182, 1.0, v182
	v_mul_f32_e32 v190, 0x3fcc422a, v190
	v_mul_f32_e32 v191, 0x3fcc422a, v191
	v_mul_f32_e32 v192, 0x3fcc422a, v192
	v_add_f32_e32 v184, 1.0, v184
	v_add_f32_e32 v186, 1.0, v186
	v_rcp_f32_e32 v33, v33
	v_rcp_f32_e32 v180, v180
	v_rcp_f32_e32 v182, v182
	v_mul_f32_e32 v190, 0xbfb8aa3b, v190
	v_mul_f32_e32 v191, 0xbfb8aa3b, v191
	v_mul_f32_e32 v192, 0xbfb8aa3b, v192
	v_rcp_f32_e32 v184, v184
	v_rcp_f32_e32 v186, v186
	v_exp_f32_e32 v190, v190
	v_exp_f32_e32 v191, v191
	v_exp_f32_e32 v192, v192
	v_mul_f32_e32 v21, v21, v33
	v_mul_f32_e32 v33, v183, v180
	v_mul_f32_e32 v180, v30, v182
	v_mul_f32_e32 v181, v181, v184
	v_mul_f32_e32 v182, v31, v186
	v_cvt_pk_bf16_f32 v30, v21, v33
	v_cvt_pk_bf16_f32 v31, v180, v181
	v_lshl_add_u32 v180, v20, 6, v29
	v_add_f32_e32 v190, 1.0, v190
	v_add_f32_e32 v191, 1.0, v191
	v_add_f32_e32 v192, 1.0, v192
	v_ashrrev_i32_e32 v181, 31, v180
	v_rcp_f32_e32 v190, v190
	v_rcp_f32_e32 v191, v191
	v_rcp_f32_e32 v192, v192
	v_lshlrev_b64 v[180:181], 10, v[180:181]
	v_lshl_add_u64 v[180:181], s[24:25], 0, v[180:181]
	v_lshl_add_u64 v[180:181], s[2:3], 1, v[180:181]
	v_lshl_add_u64 v[180:181], v[180:181], 0, v[170:171]
	v_mul_f32_e32 v183, v187, v190
	v_mul_f32_e32 v184, v32, v191
	v_mul_f32_e32 v185, v185, v192
	v_cvt_pk_bf16_f32 v32, v182, v183
	v_cvt_pk_bf16_f32 v33, v184, v185
	global_store_dwordx4 v[180:181], v[30:33], off
; #define GAS __attribute__((address_space(1)))
; __device__ __forceinline__ float gelu_tanh(float y) { const float a = 1.5957691216f * (y + 0.044715f * y * y * y); return y * sigmoidf_(a); }
; __device__ __forceinline__ unsigned cvt_pk_bf16(float lo, float hi) { unsigned r; asm volatile("v_cvt_pk_bf16_f32 %0, %1, %2" : "=v"(r) : "v"(lo), "v"(hi)); return r; }
;     __device__ __forceinline__ void operator()(const f32x4 (&acc)[2][2][4][2], const Unit& u, int wr, int wc, int fr, int fq) const {
;     ...
;                 for (int m = 0; m < 4; ++m) { const int inst = inst0 + ai * 128 + m * 16;
;                     if (inst < MT / 64) {
;                         const v4u uu = *(const GAS v4u*)(u2 + ((size_t)(g * NINST + inst) * KS2 + cidx));
;                         const f32x4 a0 = acc[ai][bj][m][0] * S5_INV, a1 = acc[ai][bj][m][1] * S5_INV;
;                         const float y0 = a0[0] + d0[0] * bflo(uu.x), y1 = a0[1] + d0[1] * bfhi(uu.x), y2 = a0[2] + d0[2] * bflo(uu.y), y3 = a0[3] + d0[3] * bfhi(uu.y);
;                         const float y4 = a1[0] + d1[0] * bflo(uu.z), y5 = a1[1] + d1[1] * bfhi(uu.z), y6 = a1[2] + d1[2] * bflo(uu.w), y7 = a1[3] + d1[3] * bfhi(uu.w);
;                         v4u w; w.x = pg8::cvt_pk_bf16(gelu_tanh(y0), gelu_tanh(y1)); w.y = pg8::cvt_pk_bf16(gelu_tanh(y2), gelu_tanh(y3));
;                         w.z = pg8::cvt_pk_bf16(gelu_tanh(y4), gelu_tanh(y5)); w.w = pg8::cvt_pk_bf16(gelu_tanh(y6), gelu_tanh(y7));
;                         *(GAS v4u*)(z + ((size_t)(inst * 64 + t) * DSSM + g * 16 + o0)) = w; } } }
.LBB0_556:
	s_or_b64 exec, exec, s[16:17]
	v_add_u32_e32 v21, 0xb0, v14
	v_cmp_gt_i32_e64 s[16:17], s70, v14
	v_add_u32_e32 v30, s20, v21
	s_and_saveexec_b64 s[20:21], s[16:17]
	s_cbranch_execz .LBB0_558
	v_mov_b64_e32 v[32:33], s[22:23]
	v_mad_i64_i32 v[32:33], s[74:75], v30, s66, v[32:33]
	v_lshl_add_u64 v[32:33], v[10:11], 1, v[32:33]
	v_mov_b64_e32 v[180:181], v[224:225]
	v_mov_b64_e32 v[182:183], v[226:227]
	v_pk_mul_f32 v[32:33], v[72:73], s[36:37] op_sel_hi:[1,0]
	v_pk_mul_f32 v[184:185], v[70:71], s[36:37] op_sel_hi:[1,0]
	v_pk_mul_f32 v[186:187], v[68:69], s[36:37] op_sel_hi:[1,0]
	v_pk_mul_f32 v[190:191], v[66:67], s[36:37] op_sel_hi:[1,0]
	s_nop 0
	v_lshlrev_b32_e32 v31, 16, v180
	v_and_b32_e32 v180, 0xffff0000, v180
	v_lshlrev_b32_e32 v192, 16, v181
	v_and_b32_e32 v181, 0xffff0000, v181
	v_lshlrev_b32_e32 v193, 16, v182
	v_and_b32_e32 v182, 0xffff0000, v182
	v_lshlrev_b32_e32 v194, 16, v183
	v_fma_f32 v6, v6, v31, v184
	v_fmac_f32_e32 v185, v7, v180
	v_fma_f32 v7, v8, v192, v32
	v_and_b32_e32 v183, 0xffff0000, v183
	v_fmac_f32_e32 v33, v9, v181
	v_fma_f32 v2, v2, v193, v190
	v_fmac_f32_e32 v191, v3, v182
	v_fma_f32 v3, v4, v194, v186
	v_mul_f32_e32 v4, 0x3d372713, v6
	v_mul_f32_e32 v8, 0x3d372713, v7
	v_fmac_f32_e32 v187, v5, v183
	v_mul_f32_e32 v5, 0x3d372713, v185
	v_mul_f32_e32 v9, 0x3d372713, v33
	v_mul_f32_e32 v31, 0x3d372713, v2
	v_mul_f32_e32 v180, 0x3d372713, v3
	v_mul_f32_e32 v4, v6, v4
	v_mul_f32_e32 v8, v7, v8
	v_mul_f32_e32 v5, v185, v5
	v_mul_f32_e32 v9, v33, v9
	v_mul_f32_e32 v31, v2, v31
	v_mul_f32_e32 v180, v3, v180
	v_fma_f32 v4, v6, v4, v6
	v_fma_f32 v8, v7, v8, v7
	v_fma_f32 v5, v185, v5, v185
	v_fma_f32 v9, v33, v9, v33
	v_fma_f32 v31, v2, v31, v2
	v_fma_f32 v180, v3, v180, v3
	v_mul_f32_e32 v4, 0x3fcc422a, v4
	v_mul_f32_e32 v8, 0x3fcc422a, v8
	v_mul_f32_e32 v5, 0x3fcc422a, v5
	v_mul_f32_e32 v9, 0x3fcc422a, v9
	v_mul_f32_e32 v31, 0x3fcc422a, v31
	v_mul_f32_e32 v180, 0x3fcc422a, v180
	v_mul_f32_e32 v4, 0xbfb8aa3b, v4
	v_mul_f32_e32 v8, 0xbfb8aa3b, v8
	v_mul_f32_e32 v5, 0xbfb8aa3b, v5
	v_mul_f32_e32 v9, 0xbfb8aa3b, v9
	v_mul_f32_e32 v31, 0xbfb8aa3b, v31
	v_mul_f32_e32 v180, 0xbfb8aa3b, v180
	v_exp_f32_e32 v4, v4
	v_exp_f32_e32 v8, v8
	v_exp_f32_e32 v5, v5
	v_exp_f32_e32 v9, v9
	v_exp_f32_e32 v31, v31
	v_exp_f32_e32 v180, v180
	v_mul_f32_e32 v32, 0x3d372713, v191
	v_mul_f32_e32 v181, 0x3d372713, v187
	v_mul_f32_e32 v32, v191, v32
	v_mul_f32_e32 v181, v187, v181
	v_fma_f32 v32, v191, v32, v191
	v_fma_f32 v181, v187, v181, v187
	v_add_f32_e32 v4, 1.0, v4
	v_add_f32_e32 v8, 1.0, v8
	v_mul_f32_e32 v32, 0x3fcc422a, v32
	v_mul_f32_e32 v181, 0x3fcc422a, v181
	v_add_f32_e32 v5, 1.0, v5
	v_add_f32_e32 v9, 1.0, v9
	v_add_f32_e32 v31, 1.0, v31
	v_add_f32_e32 v180, 1.0, v180
	v_rcp_f32_e32 v4, v4
	v_rcp_f32_e32 v8, v8
	v_mul_f32_e32 v32, 0xbfb8aa3b, v32
	v_mul_f32_e32 v181, 0xbfb8aa3b, v181
	v_rcp_f32_e32 v5, v5
	v_rcp_f32_e32 v9, v9
	v_rcp_f32_e32 v31, v31
	v_rcp_f32_e32 v180, v180
	v_exp_f32_e32 v32, v32
	v_exp_f32_e32 v181, v181
	v_mul_f32_e32 v4, v6, v4
	v_mul_f32_e32 v6, v7, v8
	v_mul_f32_e32 v5, v185, v5
	v_mul_f32_e32 v7, v33, v9
	v_mul_f32_e32 v8, v2, v31
	v_mul_f32_e32 v31, v3, v180
	v_cvt_pk_bf16_f32 v2, v4, v5
	v_cvt_pk_bf16_f32 v3, v6, v7
	v_lshl_add_u32 v6, v21, 6, v29
	v_add_f32_e32 v32, 1.0, v32
	v_add_f32_e32 v181, 1.0, v181
	v_ashrrev_i32_e32 v7, 31, v6
	v_rcp_f32_e32 v32, v32
	v_rcp_f32_e32 v181, v181
	v_lshlrev_b64 v[6:7], 10, v[6:7]
	v_lshl_add_u64 v[6:7], s[24:25], 0, v[6:7]
	v_lshl_add_u64 v[6:7], s[2:3], 1, v[6:7]
	v_lshl_add_u64 v[6:7], v[6:7], 0, v[170:171]
	v_mul_f32_e32 v9, v191, v32
	v_mul_f32_e32 v32, v187, v181
	v_cvt_pk_bf16_f32 v4, v8, v9
	v_cvt_pk_bf16_f32 v5, v31, v32
	global_store_dwordx4 v[6:7], v[2:5], off
; #define GAS __attribute__((address_space(1)))
; __device__ __forceinline__ float gelu_tanh(float y) { const float a = 1.5957691216f * (y + 0.044715f * y * y * y); return y * sigmoidf_(a); }
; __device__ __forceinline__ unsigned cvt_pk_bf16(float lo, float hi) { unsigned r; asm volatile("v_cvt_pk_bf16_f32 %0, %1, %2" : "=v"(r) : "v"(lo), "v"(hi)); return r; }
;     __device__ __forceinline__ void operator()(const f32x4 (&acc)[2][2][4][2], const Unit& u, int wr, int wc, int fr, int fq) const {
;     ...
;         for (int bj = 0; bj < 2; ++bj) { const int cidx = c0 + bj * 128, t = cidx >> 4, o0 = cidx & 15;
;             const f32x4 d0 = *(const GAS f32x4*)(dsk + g * 16 + o0), d1 = *(const GAS f32x4*)(dsk + g * 16 + o0 + 4);
; #pragma unroll
;             for (int ai = 0; ai < 2; ++ai)
; #pragma unroll
;                 for (int m = 0; m < 4; ++m) { const int inst = inst0 + ai * 128 + m * 16;
;                     if (inst < MT / 64) {
;                         const v4u uu = *(const GAS v4u*)(u2 + ((size_t)(g * NINST + inst) * KS2 + cidx));
;                         const f32x4 a0 = acc[ai][bj][m][0] * S5_INV, a1 = acc[ai][bj][m][1] * S5_INV;
;                         const float y0 = a0[0] + d0[0] * bflo(uu.x), y1 = a0[1] + d0[1] * bfhi(uu.x), y2 = a0[2] + d0[2] * bflo(uu.y), y3 = a0[3] + d0[3] * bfhi(uu.y);
;                         const float y4 = a1[0] + d1[0] * bflo(uu.z), y5 = a1[1] + d1[1] * bfhi(uu.z), y6 = a1[2] + d1[2] * bflo(uu.w), y7 = a1[3] + d1[3] * bfhi(uu.w);
;                         v4u w; w.x = pg8::cvt_pk_bf16(gelu_tanh(y0), gelu_tanh(y1)); w.y = pg8::cvt_pk_bf16(gelu_tanh(y2), gelu_tanh(y3));
;                         w.z = pg8::cvt_pk_bf16(gelu_tanh(y4), gelu_tanh(y5)); w.w = pg8::cvt_pk_bf16(gelu_tanh(y6), gelu_tanh(y7));
;                         *(GAS v4u*)(z + ((size_t)(inst * 64 + t) * DSSM + g * 16 + o0)) = w; } } }
.LBB0_558:
	s_or_b64 exec, exec, s[20:21]
	global_load_dwordx4 v[6:9], v[12:13], off
	global_load_dwordx4 v[2:5], v[12:13], off offset:16
	s_waitcnt vmcnt(0)
	v_or_b32_e32 v12, 0x80, v10
	v_ashrrev_i32_e32 v12, 4, v12
	s_and_saveexec_b64 s[20:21], vcc
	s_cbranch_execz .LBB0_567
	v_mov_b64_e32 v[32:33], s[22:23]
	v_mad_i64_i32 v[32:33], s[74:75], v22, s66, v[32:33]
	v_lshl_add_u64 v[32:33], v[10:11], 1, v[32:33]
	v_mov_b64_e32 v[180:181], v[228:229]
	v_mov_b64_e32 v[182:183], v[230:231]
	v_pk_mul_f32 v[184:185], v[126:127], s[36:37] op_sel_hi:[1,0]
	v_pk_mul_f32 v[32:33], v[128:129], s[36:37] op_sel_hi:[1,0]
	v_pk_mul_f32 v[190:191], v[122:123], s[36:37] op_sel_hi:[1,0]
	v_pk_mul_f32 v[186:187], v[124:125], s[36:37] op_sel_hi:[1,0]
	s_nop 0
	v_lshlrev_b32_e32 v13, 16, v180
	v_and_b32_e32 v22, 0xffff0000, v180
	v_lshlrev_b32_e32 v29, 16, v181
	v_and_b32_e32 v31, 0xffff0000, v181
	v_lshlrev_b32_e32 v180, 16, v182
	v_fma_f32 v13, v6, v13, v184
	v_fmac_f32_e32 v185, v7, v22
	v_and_b32_e32 v181, 0xffff0000, v182
	v_lshlrev_b32_e32 v182, 16, v183
	v_fma_f32 v22, v8, v29, v32
	v_fmac_f32_e32 v33, v9, v31
	v_fma_f32 v29, v2, v180, v190
	v_mul_f32_e32 v32, 0x3d372713, v13
	v_mul_f32_e32 v180, 0x3d372713, v185
	v_fma_f32 v31, v4, v182, v186
	v_mul_f32_e32 v182, 0x3d372713, v33
	v_mul_f32_e32 v32, v13, v32
	v_mul_f32_e32 v180, v185, v180
	v_fmac_f32_e32 v191, v3, v181
	v_mul_f32_e32 v181, 0x3d372713, v22
	v_mul_f32_e32 v182, v33, v182
	v_fma_f32 v32, v13, v32, v13
	v_fma_f32 v180, v185, v180, v185
	v_mul_f32_e32 v181, v22, v181
	v_fma_f32 v182, v33, v182, v33
	v_mul_f32_e32 v32, 0x3fcc422a, v32
	v_mul_f32_e32 v180, 0x3fcc422a, v180
	v_and_b32_e32 v183, 0xffff0000, v183
	v_fma_f32 v181, v22, v181, v22
	v_mul_f32_e32 v182, 0x3fcc422a, v182
	v_mul_f32_e32 v32, 0xbfb8aa3b, v32
	v_mul_f32_e32 v180, 0xbfb8aa3b, v180
	v_fmac_f32_e32 v187, v5, v183
	v_mul_f32_e32 v181, 0x3fcc422a, v181
	v_mul_f32_e32 v182, 0xbfb8aa3b, v182
	v_exp_f32_e32 v32, v32
	v_exp_f32_e32 v180, v180
	v_mul_f32_e32 v183, 0x3d372713, v29
	v_mul_f32_e32 v184, 0x3d372713, v191
	v_mul_f32_e32 v190, 0x3d372713, v187
	v_mul_f32_e32 v181, 0xbfb8aa3b, v181
	v_exp_f32_e32 v182, v182
	v_mul_f32_e32 v186, 0x3d372713, v31
	v_mul_f32_e32 v183, v29, v183
	v_mul_f32_e32 v184, v191, v184
	v_mul_f32_e32 v190, v187, v190
	v_exp_f32_e32 v181, v181
	v_mul_f32_e32 v186, v31, v186
	v_fma_f32 v183, v29, v183, v29
	v_fma_f32 v184, v191, v184, v191
	v_fma_f32 v190, v187, v190, v187
	v_fma_f32 v186, v31, v186, v31
	v_mul_f32_e32 v183, 0x3fcc422a, v183
	v_mul_f32_e32 v184, 0x3fcc422a, v184
	v_mul_f32_e32 v190, 0x3fcc422a, v190
	v_add_f32_e32 v32, 1.0, v32
	v_add_f32_e32 v180, 1.0, v180
	v_mul_f32_e32 v186, 0x3fcc422a, v186
	v_mul_f32_e32 v183, 0xbfb8aa3b, v183
	v_mul_f32_e32 v184, 0xbfb8aa3b, v184
	v_mul_f32_e32 v190, 0xbfb8aa3b, v190
	v_add_f32_e32 v182, 1.0, v182
	v_rcp_f32_e32 v32, v32
	v_rcp_f32_e32 v180, v180
	v_mul_f32_e32 v186, 0xbfb8aa3b, v186
	v_exp_f32_e32 v183, v183
	v_exp_f32_e32 v184, v184
	v_exp_f32_e32 v190, v190
	v_add_f32_e32 v181, 1.0, v181
	v_rcp_f32_e32 v182, v182
	v_exp_f32_e32 v186, v186
	v_rcp_f32_e32 v181, v181
	v_mul_f32_e32 v13, v13, v32
	v_mul_f32_e32 v32, v185, v180
	v_add_f32_e32 v183, 1.0, v183
	v_add_f32_e32 v184, 1.0, v184
	v_add_f32_e32 v190, 1.0, v190
	v_mul_f32_e32 v33, v33, v182
	v_cvt_pk_bf16_f32 v180, v13, v32
	v_lshl_add_u32 v32, v14, 6, v12
	v_add_f32_e32 v186, 1.0, v186
	v_rcp_f32_e32 v183, v183
	v_rcp_f32_e32 v184, v184
	v_rcp_f32_e32 v190, v190
	v_mul_f32_e32 v22, v22, v181
	v_cvt_pk_bf16_f32 v181, v22, v33
	v_ashrrev_i32_e32 v33, 31, v32
	v_rcp_f32_e32 v186, v186
	v_lshlrev_b64 v[32:33], 10, v[32:33]
	v_lshl_add_u64 v[32:33], s[24:25], 0, v[32:33]
	v_lshl_add_u64 v[32:33], s[2:3], 1, v[32:33]
	v_mul_f32_e32 v29, v29, v183
	v_mul_f32_e32 v182, v191, v184
	v_mul_f32_e32 v183, v187, v190
	v_lshl_add_u64 v[32:33], v[32:33], 0, v[170:171]
	v_mul_f32_e32 v31, v31, v186
	v_cvt_pk_bf16_f32 v182, v29, v182
	v_cvt_pk_bf16_f32 v183, v31, v183
	global_store_dwordx4 v[32:33], v[180:183], off
	s_or_b64 exec, exec, s[20:21]
	s_and_saveexec_b64 s[20:21], s[4:5]
	s_cbranch_execnz .LBB0_568

; #define GAS __attribute__((address_space(1)))
; __device__ __forceinline__ float gelu_tanh(float y) { const float a = 1.5957691216f * (y + 0.044715f * y * y * y); return y * sigmoidf_(a); }
; __device__ __forceinline__ unsigned cvt_pk_bf16(float lo, float hi) { unsigned r; asm volatile("v_cvt_pk_bf16_f32 %0, %1, %2" : "=v"(r) : "v"(lo), "v"(hi)); return r; }
;     __device__ __forceinline__ void operator()(const f32x4 (&acc)[2][2][4][2], const Unit& u, int wr, int wc, int fr, int fq) const {
;     ...
;                 for (int m = 0; m < 4; ++m) { const int inst = inst0 + ai * 128 + m * 16;
;                     if (inst < MT / 64) {
;                         const v4u uu = *(const GAS v4u*)(u2 + ((size_t)(g * NINST + inst) * KS2 + cidx));
;                         const f32x4 a0 = acc[ai][bj][m][0] * S5_INV, a1 = acc[ai][bj][m][1] * S5_INV;
;                         const float y0 = a0[0] + d0[0] * bflo(uu.x), y1 = a0[1] + d0[1] * bfhi(uu.x), y2 = a0[2] + d0[2] * bflo(uu.y), y3 = a0[3] + d0[3] * bfhi(uu.y);
;                         const float y4 = a1[0] + d1[0] * bflo(uu.z), y5 = a1[1] + d1[1] * bfhi(uu.z), y6 = a1[2] + d1[2] * bflo(uu.w), y7 = a1[3] + d1[3] * bfhi(uu.w);
;                         v4u w; w.x = pg8::cvt_pk_bf16(gelu_tanh(y0), gelu_tanh(y1)); w.y = pg8::cvt_pk_bf16(gelu_tanh(y2), gelu_tanh(y3));
;                         w.z = pg8::cvt_pk_bf16(gelu_tanh(y4), gelu_tanh(y5)); w.w = pg8::cvt_pk_bf16(gelu_tanh(y6), gelu_tanh(y7));
;                         *(GAS v4u*)(z + ((size_t)(inst * 64 + t) * DSSM + g * 16 + o0)) = w; } } }
.LBB0_561:
	v_mov_b64_e32 v[14:15], s[22:23]
	v_mad_i64_i32 v[14:15], s[6:7], v24, s66, v[14:15]
	v_lshl_add_u64 v[14:15], v[10:11], 1, v[14:15]
	v_mov_b64_e32 v[180:181], v[232:233]
	v_mov_b64_e32 v[182:183], v[234:235]
	v_pk_mul_f32 v[14:15], v[112:113], s[36:37] op_sel_hi:[1,0]
	v_pk_mul_f32 v[22:23], v[110:111], s[36:37] op_sel_hi:[1,0]
	v_pk_mul_f32 v[32:33], v[108:109], s[36:37] op_sel_hi:[1,0]
	v_pk_mul_f32 v[184:185], v[106:107], s[36:37] op_sel_hi:[1,0]
	s_nop 0
	v_lshlrev_b32_e32 v29, 16, v181
	v_lshlrev_b32_e32 v13, 16, v180
	v_and_b32_e32 v24, 0xffff0000, v180
	v_and_b32_e32 v31, 0xffff0000, v181
	v_lshlrev_b32_e32 v180, 16, v182
	v_and_b32_e32 v181, 0xffff0000, v182
	v_lshlrev_b32_e32 v182, 16, v183
	v_fma_f32 v14, v8, v29, v14
	v_fma_f32 v13, v6, v13, v22
	v_fmac_f32_e32 v23, v7, v24
	v_fmac_f32_e32 v15, v9, v31
	v_fma_f32 v22, v2, v180, v184
	v_fma_f32 v24, v4, v182, v32
	v_mul_f32_e32 v32, 0x3d372713, v14
	v_fmac_f32_e32 v185, v3, v181
	v_mul_f32_e32 v29, 0x3d372713, v13
	v_mul_f32_e32 v31, 0x3d372713, v23
	v_mul_f32_e32 v180, 0x3d372713, v15
	v_mul_f32_e32 v181, 0x3d372713, v22
	v_mul_f32_e32 v32, v14, v32
	v_mul_f32_e32 v29, v13, v29
	v_mul_f32_e32 v31, v23, v31
	v_mul_f32_e32 v180, v15, v180
	v_mul_f32_e32 v181, v22, v181
	v_fma_f32 v32, v14, v32, v14
	v_fma_f32 v29, v13, v29, v13
	v_fma_f32 v31, v23, v31, v23
	v_fma_f32 v180, v15, v180, v15
	v_fma_f32 v181, v22, v181, v22
	v_mul_f32_e32 v32, 0x3fcc422a, v32
	v_mul_f32_e32 v29, 0x3fcc422a, v29
	v_mul_f32_e32 v31, 0x3fcc422a, v31
	v_mul_f32_e32 v180, 0x3fcc422a, v180
	v_mul_f32_e32 v181, 0x3fcc422a, v181
	v_mul_f32_e32 v32, 0xbfb8aa3b, v32
	v_and_b32_e32 v183, 0xffff0000, v183
	v_mul_f32_e32 v29, 0xbfb8aa3b, v29
	v_mul_f32_e32 v31, 0xbfb8aa3b, v31
	v_mul_f32_e32 v180, 0xbfb8aa3b, v180
	v_mul_f32_e32 v181, 0xbfb8aa3b, v181
	v_exp_f32_e32 v32, v32
	v_fmac_f32_e32 v33, v5, v183
	v_exp_f32_e32 v29, v29
	v_exp_f32_e32 v31, v31
	v_exp_f32_e32 v180, v180
	v_exp_f32_e32 v181, v181
	v_mul_f32_e32 v182, 0x3d372713, v185
	v_mul_f32_e32 v183, 0x3d372713, v24
	v_mul_f32_e32 v184, 0x3d372713, v33
	v_mul_f32_e32 v182, v185, v182
	v_mul_f32_e32 v183, v24, v183
	v_mul_f32_e32 v184, v33, v184
	v_fma_f32 v182, v185, v182, v185
	v_fma_f32 v183, v24, v183, v24
	v_fma_f32 v184, v33, v184, v33
	v_add_f32_e32 v32, 1.0, v32
	v_mul_f32_e32 v182, 0x3fcc422a, v182
	v_mul_f32_e32 v183, 0x3fcc422a, v183
	v_mul_f32_e32 v184, 0x3fcc422a, v184
	v_add_f32_e32 v29, 1.0, v29
	v_add_f32_e32 v31, 1.0, v31
	v_add_f32_e32 v180, 1.0, v180
	v_add_f32_e32 v181, 1.0, v181
	v_rcp_f32_e32 v32, v32
	v_mul_f32_e32 v182, 0xbfb8aa3b, v182
	v_mul_f32_e32 v183, 0xbfb8aa3b, v183
	v_mul_f32_e32 v184, 0xbfb8aa3b, v184
	v_rcp_f32_e32 v29, v29
	v_rcp_f32_e32 v31, v31
	v_rcp_f32_e32 v180, v180
	v_rcp_f32_e32 v181, v181
	v_exp_f32_e32 v182, v182
	v_exp_f32_e32 v183, v183
	v_exp_f32_e32 v184, v184
	v_mul_f32_e32 v14, v14, v32
	v_mul_f32_e32 v13, v13, v29
	v_mul_f32_e32 v23, v23, v31
	v_mul_f32_e32 v15, v15, v180
	v_mul_f32_e32 v22, v22, v181
	v_cvt_pk_bf16_f32 v180, v13, v23
	v_cvt_pk_bf16_f32 v181, v14, v15
	v_lshl_add_u32 v14, v16, 6, v12
	v_add_f32_e32 v182, 1.0, v182
	v_add_f32_e32 v183, 1.0, v183
	v_add_f32_e32 v184, 1.0, v184
	v_ashrrev_i32_e32 v15, 31, v14
	v_rcp_f32_e32 v182, v182
	v_rcp_f32_e32 v183, v183
	v_rcp_f32_e32 v184, v184
	v_lshlrev_b64 v[14:15], 10, v[14:15]
	v_lshl_add_u64 v[14:15], s[24:25], 0, v[14:15]
	v_lshl_add_u64 v[14:15], s[2:3], 1, v[14:15]
	v_lshl_add_u64 v[14:15], v[14:15], 0, v[170:171]
	v_mul_f32_e32 v29, v185, v182
	v_mul_f32_e32 v24, v24, v183
	v_mul_f32_e32 v31, v33, v184
	v_cvt_pk_bf16_f32 v182, v22, v29
	v_cvt_pk_bf16_f32 v183, v24, v31
	global_store_dwordx4 v[14:15], v[180:183], off
	s_or_b64 exec, exec, s[4:5]
	s_and_saveexec_b64 s[4:5], s[8:9]
	s_cbranch_execnz .LBB0_570

; #define GAS __attribute__((address_space(1)))
; __device__ __forceinline__ float gelu_tanh(float y) { const float a = 1.5957691216f * (y + 0.044715f * y * y * y); return y * sigmoidf_(a); }
; __device__ __forceinline__ unsigned cvt_pk_bf16(float lo, float hi) { unsigned r; asm volatile("v_cvt_pk_bf16_f32 %0, %1, %2" : "=v"(r) : "v"(lo), "v"(hi)); return r; }
;     __device__ __forceinline__ void operator()(const f32x4 (&acc)[2][2][4][2], const Unit& u, int wr, int wc, int fr, int fq) const {
;     ...
;                 for (int m = 0; m < 4; ++m) { const int inst = inst0 + ai * 128 + m * 16;
;                     if (inst < MT / 64) {
;                         const v4u uu = *(const GAS v4u*)(u2 + ((size_t)(g * NINST + inst) * KS2 + cidx));
;                         const f32x4 a0 = acc[ai][bj][m][0] * S5_INV, a1 = acc[ai][bj][m][1] * S5_INV;
;                         const float y0 = a0[0] + d0[0] * bflo(uu.x), y1 = a0[1] + d0[1] * bfhi(uu.x), y2 = a0[2] + d0[2] * bflo(uu.y), y3 = a0[3] + d0[3] * bfhi(uu.y);
;                         const float y4 = a1[0] + d1[0] * bflo(uu.z), y5 = a1[1] + d1[1] * bfhi(uu.z), y6 = a1[2] + d1[2] * bflo(uu.w), y7 = a1[3] + d1[3] * bfhi(uu.w);
;                         v4u w; w.x = pg8::cvt_pk_bf16(gelu_tanh(y0), gelu_tanh(y1)); w.y = pg8::cvt_pk_bf16(gelu_tanh(y2), gelu_tanh(y3));
;                         w.z = pg8::cvt_pk_bf16(gelu_tanh(y4), gelu_tanh(y5)); w.w = pg8::cvt_pk_bf16(gelu_tanh(y6), gelu_tanh(y7));
;                         *(GAS v4u*)(z + ((size_t)(inst * 64 + t) * DSSM + g * 16 + o0)) = w; } } }
.LBB0_563:
	v_mov_b64_e32 v[14:15], s[22:23]
	v_mad_i64_i32 v[14:15], s[6:7], v26, s66, v[14:15]
	v_lshl_add_u64 v[14:15], v[10:11], 1, v[14:15]
	v_mov_b64_e32 v[14:15], v[240:241]
	v_mov_b64_e32 v[16:17], v[242:243]
	v_pk_mul_f32 v[22:23], v[64:65], s[36:37] op_sel_hi:[1,0]
	v_pk_mul_f32 v[24:25], v[62:63], s[36:37] op_sel_hi:[1,0]
	v_pk_mul_f32 v[32:33], v[60:61], s[36:37] op_sel_hi:[1,0]
	v_pk_mul_f32 v[180:181], v[58:59], s[36:37] op_sel_hi:[1,0]
	s_nop 0
	v_lshlrev_b32_e32 v13, 16, v14
	v_and_b32_e32 v14, 0xffff0000, v14
	v_lshlrev_b32_e32 v26, 16, v15
	v_and_b32_e32 v15, 0xffff0000, v15
	v_lshlrev_b32_e32 v29, 16, v16
	v_lshlrev_b32_e32 v31, 16, v17
	v_and_b32_e32 v17, 0xffff0000, v17
	v_fma_f32 v13, v6, v13, v24
	v_fmac_f32_e32 v25, v7, v14
	v_fma_f32 v14, v8, v26, v22
	v_fmac_f32_e32 v23, v9, v15
	v_fma_f32 v15, v2, v29, v180
	v_fmac_f32_e32 v33, v5, v17
	v_mul_f32_e32 v17, 0x3d372713, v13
	v_mul_f32_e32 v22, 0x3d372713, v25
	v_mul_f32_e32 v24, 0x3d372713, v14
	v_mul_f32_e32 v26, 0x3d372713, v23
	v_mul_f32_e32 v29, 0x3d372713, v15
	v_mul_f32_e32 v17, v13, v17
	v_mul_f32_e32 v22, v25, v22
	v_mul_f32_e32 v24, v14, v24
	v_mul_f32_e32 v26, v23, v26
	v_mul_f32_e32 v29, v15, v29
	v_fma_f32 v17, v13, v17, v13
	v_fma_f32 v22, v25, v22, v25
	v_fma_f32 v24, v14, v24, v14
	v_fma_f32 v26, v23, v26, v23
	v_fma_f32 v29, v15, v29, v15
	v_mul_f32_e32 v17, 0x3fcc422a, v17
	v_mul_f32_e32 v22, 0x3fcc422a, v22
	v_mul_f32_e32 v24, 0x3fcc422a, v24
	v_mul_f32_e32 v26, 0x3fcc422a, v26
	v_mul_f32_e32 v29, 0x3fcc422a, v29
	v_mul_f32_e32 v17, 0xbfb8aa3b, v17
	v_mul_f32_e32 v22, 0xbfb8aa3b, v22
	v_mul_f32_e32 v24, 0xbfb8aa3b, v24
	v_and_b32_e32 v16, 0xffff0000, v16
	v_mul_f32_e32 v26, 0xbfb8aa3b, v26
	v_mul_f32_e32 v29, 0xbfb8aa3b, v29
	v_exp_f32_e32 v17, v17
	v_exp_f32_e32 v22, v22
	v_exp_f32_e32 v24, v24
	v_fmac_f32_e32 v181, v3, v16
	v_fma_f32 v16, v4, v31, v32
	v_exp_f32_e32 v26, v26
	v_exp_f32_e32 v29, v29
	v_mul_f32_e32 v31, 0x3d372713, v181
	v_mul_f32_e32 v32, 0x3d372713, v16
	v_mul_f32_e32 v180, 0x3d372713, v33
	v_mul_f32_e32 v31, v181, v31
	v_mul_f32_e32 v32, v16, v32
	v_mul_f32_e32 v180, v33, v180
	v_fma_f32 v31, v181, v31, v181
	v_fma_f32 v32, v16, v32, v16
	v_fma_f32 v180, v33, v180, v33
	v_add_f32_e32 v17, 1.0, v17
	v_add_f32_e32 v22, 1.0, v22
	v_add_f32_e32 v24, 1.0, v24
	v_mul_f32_e32 v31, 0x3fcc422a, v31
	v_mul_f32_e32 v32, 0x3fcc422a, v32
	v_mul_f32_e32 v180, 0x3fcc422a, v180
	v_add_f32_e32 v26, 1.0, v26
	v_add_f32_e32 v29, 1.0, v29
	v_rcp_f32_e32 v17, v17
	v_rcp_f32_e32 v22, v22
	v_rcp_f32_e32 v24, v24
	v_mul_f32_e32 v31, 0xbfb8aa3b, v31
	v_mul_f32_e32 v32, 0xbfb8aa3b, v32
	v_mul_f32_e32 v180, 0xbfb8aa3b, v180
	v_rcp_f32_e32 v26, v26
	v_rcp_f32_e32 v29, v29
	v_exp_f32_e32 v31, v31
	v_exp_f32_e32 v32, v32
	v_exp_f32_e32 v180, v180
	v_mul_f32_e32 v13, v13, v17
	v_mul_f32_e32 v17, v25, v22
	v_mul_f32_e32 v22, v14, v24
	v_mul_f32_e32 v23, v23, v26
	v_mul_f32_e32 v24, v15, v29
	v_cvt_pk_bf16_f32 v14, v13, v17
	v_cvt_pk_bf16_f32 v15, v22, v23
	v_lshl_add_u32 v22, v18, 6, v12
	v_add_f32_e32 v31, 1.0, v31
	v_add_f32_e32 v32, 1.0, v32
	v_add_f32_e32 v180, 1.0, v180
	v_ashrrev_i32_e32 v23, 31, v22
	v_rcp_f32_e32 v31, v31
	v_rcp_f32_e32 v32, v32
	v_rcp_f32_e32 v180, v180
	v_lshlrev_b64 v[22:23], 10, v[22:23]
	v_lshl_add_u64 v[22:23], s[24:25], 0, v[22:23]
	v_lshl_add_u64 v[22:23], s[2:3], 1, v[22:23]
	v_lshl_add_u64 v[22:23], v[22:23], 0, v[170:171]
	v_mul_f32_e32 v25, v181, v31
	v_mul_f32_e32 v26, v16, v32
	v_mul_f32_e32 v29, v33, v180
	v_cvt_pk_bf16_f32 v16, v24, v25
	v_cvt_pk_bf16_f32 v17, v26, v29
	global_store_dwordx4 v[22:23], v[14:17], off
	s_or_b64 exec, exec, s[4:5]
	s_and_saveexec_b64 s[4:5], s[12:13]
	s_cbranch_execnz .LBB0_572

; #define GAS __attribute__((address_space(1)))
; __device__ __forceinline__ float gelu_tanh(float y) { const float a = 1.5957691216f * (y + 0.044715f * y * y * y); return y * sigmoidf_(a); }
; __device__ __forceinline__ unsigned cvt_pk_bf16(float lo, float hi) { unsigned r; asm volatile("v_cvt_pk_bf16_f32 %0, %1, %2" : "=v"(r) : "v"(lo), "v"(hi)); return r; }
;     __device__ __forceinline__ void operator()(const f32x4 (&acc)[2][2][4][2], const Unit& u, int wr, int wc, int fr, int fq) const {
;     ...
;                 for (int m = 0; m < 4; ++m) { const int inst = inst0 + ai * 128 + m * 16;
;                     if (inst < MT / 64) {
;                         const v4u uu = *(const GAS v4u*)(u2 + ((size_t)(g * NINST + inst) * KS2 + cidx));
;                         const f32x4 a0 = acc[ai][bj][m][0] * S5_INV, a1 = acc[ai][bj][m][1] * S5_INV;
;                         const float y0 = a0[0] + d0[0] * bflo(uu.x), y1 = a0[1] + d0[1] * bfhi(uu.x), y2 = a0[2] + d0[2] * bflo(uu.y), y3 = a0[3] + d0[3] * bfhi(uu.y);
;                         const float y4 = a1[0] + d1[0] * bflo(uu.z), y5 = a1[1] + d1[1] * bfhi(uu.z), y6 = a1[2] + d1[2] * bflo(uu.w), y7 = a1[3] + d1[3] * bfhi(uu.w);
;                         v4u w; w.x = pg8::cvt_pk_bf16(gelu_tanh(y0), gelu_tanh(y1)); w.y = pg8::cvt_pk_bf16(gelu_tanh(y2), gelu_tanh(y3));
;                         w.z = pg8::cvt_pk_bf16(gelu_tanh(y4), gelu_tanh(y5)); w.w = pg8::cvt_pk_bf16(gelu_tanh(y6), gelu_tanh(y7));
;                         *(GAS v4u*)(z + ((size_t)(inst * 64 + t) * DSSM + g * 16 + o0)) = w; } } }
.LBB0_565:
	v_mov_b64_e32 v[14:15], s[22:23]
	v_mad_i64_i32 v[14:15], s[6:7], v28, s66, v[14:15]
	v_lshl_add_u64 v[14:15], v[10:11], 1, v[14:15]
	v_mov_b64_e32 v[14:15], v[244:245]
	v_mov_b64_e32 v[16:17], v[246:247]
	v_pk_mul_f32 v[18:19], v[48:49], s[36:37] op_sel_hi:[1,0]
	v_pk_mul_f32 v[22:23], v[46:47], s[36:37] op_sel_hi:[1,0]
	v_pk_mul_f32 v[24:25], v[44:45], s[36:37] op_sel_hi:[1,0]
	v_pk_mul_f32 v[26:27], v[42:43], s[36:37] op_sel_hi:[1,0]
	s_nop 0
	v_lshlrev_b32_e32 v13, 16, v14
	v_and_b32_e32 v14, 0xffff0000, v14
	v_lshlrev_b32_e32 v28, 16, v15
	v_and_b32_e32 v15, 0xffff0000, v15
	v_lshlrev_b32_e32 v29, 16, v16
	v_lshlrev_b32_e32 v31, 16, v17
	v_and_b32_e32 v17, 0xffff0000, v17
	v_fma_f32 v13, v6, v13, v22
	v_fmac_f32_e32 v23, v7, v14
	v_fma_f32 v14, v8, v28, v18
	v_and_b32_e32 v16, 0xffff0000, v16
	v_fmac_f32_e32 v19, v9, v15
	v_fma_f32 v15, v2, v29, v26
	v_fmac_f32_e32 v25, v5, v17
	v_mul_f32_e32 v17, 0x3d372713, v13
	v_mul_f32_e32 v18, 0x3d372713, v23
	v_mul_f32_e32 v22, 0x3d372713, v14
	v_fmac_f32_e32 v27, v3, v16
	v_fma_f32 v16, v4, v31, v24
	v_mul_f32_e32 v24, 0x3d372713, v19
	v_mul_f32_e32 v26, 0x3d372713, v15
	v_mul_f32_e32 v17, v13, v17
	v_mul_f32_e32 v18, v23, v18
	v_mul_f32_e32 v22, v14, v22
	v_mul_f32_e32 v24, v19, v24
	v_mul_f32_e32 v26, v15, v26
	v_fma_f32 v17, v13, v17, v13
	v_fma_f32 v18, v23, v18, v23
	v_fma_f32 v22, v14, v22, v14
	v_fma_f32 v24, v19, v24, v19
	v_fma_f32 v26, v15, v26, v15
	v_mul_f32_e32 v17, 0x3fcc422a, v17
	v_mul_f32_e32 v18, 0x3fcc422a, v18
	v_mul_f32_e32 v22, 0x3fcc422a, v22
	v_mul_f32_e32 v24, 0x3fcc422a, v24
	v_mul_f32_e32 v26, 0x3fcc422a, v26
	v_mul_f32_e32 v17, 0xbfb8aa3b, v17
	v_mul_f32_e32 v18, 0xbfb8aa3b, v18
	v_mul_f32_e32 v22, 0xbfb8aa3b, v22
	v_mul_f32_e32 v24, 0xbfb8aa3b, v24
	v_mul_f32_e32 v26, 0xbfb8aa3b, v26
	v_exp_f32_e32 v17, v17
	v_exp_f32_e32 v18, v18
	v_exp_f32_e32 v22, v22
	v_exp_f32_e32 v24, v24
	v_exp_f32_e32 v26, v26
	v_mul_f32_e32 v28, 0x3d372713, v27
	v_mul_f32_e32 v29, 0x3d372713, v16
	v_mul_f32_e32 v31, 0x3d372713, v25
	v_mul_f32_e32 v28, v27, v28
	v_mul_f32_e32 v29, v16, v29
	v_mul_f32_e32 v31, v25, v31
	v_fma_f32 v28, v27, v28, v27
	v_fma_f32 v29, v16, v29, v16
	v_fma_f32 v31, v25, v31, v25
	v_add_f32_e32 v17, 1.0, v17
	v_add_f32_e32 v18, 1.0, v18
	v_add_f32_e32 v22, 1.0, v22
	v_mul_f32_e32 v28, 0x3fcc422a, v28
	v_mul_f32_e32 v29, 0x3fcc422a, v29
	v_mul_f32_e32 v31, 0x3fcc422a, v31
	v_add_f32_e32 v24, 1.0, v24
	v_add_f32_e32 v26, 1.0, v26
	v_rcp_f32_e32 v17, v17
	v_rcp_f32_e32 v18, v18
	v_rcp_f32_e32 v22, v22
	v_mul_f32_e32 v28, 0xbfb8aa3b, v28
	v_mul_f32_e32 v29, 0xbfb8aa3b, v29
	v_mul_f32_e32 v31, 0xbfb8aa3b, v31
	v_rcp_f32_e32 v24, v24
	v_rcp_f32_e32 v26, v26
	v_exp_f32_e32 v28, v28
	v_exp_f32_e32 v29, v29
	v_exp_f32_e32 v31, v31
	v_mul_f32_e32 v13, v13, v17
	v_mul_f32_e32 v17, v23, v18
	v_mul_f32_e32 v18, v14, v22
	v_mul_f32_e32 v19, v19, v24
	v_mul_f32_e32 v22, v15, v26
	v_cvt_pk_bf16_f32 v14, v13, v17
	v_cvt_pk_bf16_f32 v15, v18, v19
	v_lshl_add_u32 v18, v20, 6, v12
	v_add_f32_e32 v28, 1.0, v28
	v_add_f32_e32 v29, 1.0, v29
	v_add_f32_e32 v31, 1.0, v31
	v_ashrrev_i32_e32 v19, 31, v18
	v_rcp_f32_e32 v28, v28
	v_rcp_f32_e32 v29, v29
	v_rcp_f32_e32 v31, v31
	v_lshlrev_b64 v[18:19], 10, v[18:19]
	v_lshl_add_u64 v[18:19], s[24:25], 0, v[18:19]
	v_lshl_add_u64 v[18:19], s[2:3], 1, v[18:19]
	v_lshl_add_u64 v[18:19], v[18:19], 0, v[170:171]
	v_mul_f32_e32 v23, v27, v28
	v_mul_f32_e32 v24, v16, v29
	v_mul_f32_e32 v25, v25, v31
	v_cvt_pk_bf16_f32 v16, v22, v23
	v_cvt_pk_bf16_f32 v17, v24, v25
	global_store_dwordx4 v[18:19], v[14:17], off
	s_or_b64 exec, exec, s[4:5]
	s_and_saveexec_b64 s[4:5], s[16:17]
	s_cbranch_execnz .LBB0_574

; #define GAS __attribute__((address_space(1)))
; __device__ __forceinline__ float gelu_tanh(float y) { const float a = 1.5957691216f * (y + 0.044715f * y * y * y); return y * sigmoidf_(a); }
; __device__ __forceinline__ unsigned cvt_pk_bf16(float lo, float hi) { unsigned r; asm volatile("v_cvt_pk_bf16_f32 %0, %1, %2" : "=v"(r) : "v"(lo), "v"(hi)); return r; }
;     __device__ __forceinline__ void operator()(const f32x4 (&acc)[2][2][4][2], const Unit& u, int wr, int wc, int fr, int fq) const {
;     ...
;                 for (int m = 0; m < 4; ++m) { const int inst = inst0 + ai * 128 + m * 16;
;                     if (inst < MT / 64) {
;                         const v4u uu = *(const GAS v4u*)(u2 + ((size_t)(g * NINST + inst) * KS2 + cidx));
;                         const f32x4 a0 = acc[ai][bj][m][0] * S5_INV, a1 = acc[ai][bj][m][1] * S5_INV;
;                         const float y0 = a0[0] + d0[0] * bflo(uu.x), y1 = a0[1] + d0[1] * bfhi(uu.x), y2 = a0[2] + d0[2] * bflo(uu.y), y3 = a0[3] + d0[3] * bfhi(uu.y);
;                         const float y4 = a1[0] + d1[0] * bflo(uu.z), y5 = a1[1] + d1[1] * bfhi(uu.z), y6 = a1[2] + d1[2] * bflo(uu.w), y7 = a1[3] + d1[3] * bfhi(uu.w);
;                         v4u w; w.x = pg8::cvt_pk_bf16(gelu_tanh(y0), gelu_tanh(y1)); w.y = pg8::cvt_pk_bf16(gelu_tanh(y2), gelu_tanh(y3));
;                         w.z = pg8::cvt_pk_bf16(gelu_tanh(y4), gelu_tanh(y5)); w.w = pg8::cvt_pk_bf16(gelu_tanh(y6), gelu_tanh(y7));
;                         *(GAS v4u*)(z + ((size_t)(inst * 64 + t) * DSSM + g * 16 + o0)) = w; } } }
.LBB0_568:
	v_mov_b64_e32 v[32:33], s[22:23]
	v_mad_i64_i32 v[22:23], s[4:5], v23, s66, v[32:33]
	v_lshl_add_u64 v[22:23], v[10:11], 1, v[22:23]
	v_mov_b64_e32 v[180:181], v[162:163]
	v_mov_b64_e32 v[182:183], v[164:165]
	v_pk_mul_f32 v[22:23], v[120:121], s[36:37] op_sel_hi:[1,0]
	v_pk_mul_f32 v[32:33], v[118:119], s[36:37] op_sel_hi:[1,0]
	v_pk_mul_f32 v[186:187], v[114:115], s[36:37] op_sel_hi:[1,0]
	v_pk_mul_f32 v[184:185], v[116:117], s[36:37] op_sel_hi:[1,0]
	s_nop 0
	v_and_b32_e32 v14, 0xffff0000, v180
	v_lshlrev_b32_e32 v29, 16, v181
	v_lshlrev_b32_e32 v13, 16, v180
	v_and_b32_e32 v31, 0xffff0000, v181
	v_lshlrev_b32_e32 v180, 16, v182
	v_fmac_f32_e32 v33, v7, v14
	v_fma_f32 v14, v8, v29, v22
	v_and_b32_e32 v181, 0xffff0000, v182
	v_fma_f32 v13, v6, v13, v32
	v_fmac_f32_e32 v23, v9, v31
	v_fma_f32 v22, v2, v180, v186
	v_mul_f32_e32 v180, 0x3d372713, v14
	v_fmac_f32_e32 v187, v3, v181
	v_mul_f32_e32 v31, 0x3d372713, v13
	v_mul_f32_e32 v32, 0x3d372713, v33
	v_mul_f32_e32 v181, 0x3d372713, v23
	v_mul_f32_e32 v180, v14, v180
	v_mul_f32_e32 v31, v13, v31
	v_mul_f32_e32 v32, v33, v32
	v_mul_f32_e32 v181, v23, v181
	v_fma_f32 v180, v14, v180, v14
	v_fma_f32 v31, v13, v31, v13
	v_fma_f32 v32, v33, v32, v33
	v_fma_f32 v181, v23, v181, v23
	v_mul_f32_e32 v180, 0x3fcc422a, v180
	v_mul_f32_e32 v31, 0x3fcc422a, v31
	v_mul_f32_e32 v32, 0x3fcc422a, v32
	v_mul_f32_e32 v181, 0x3fcc422a, v181
	v_mul_f32_e32 v180, 0xbfb8aa3b, v180
	v_lshlrev_b32_e32 v182, 16, v183
	v_and_b32_e32 v183, 0xffff0000, v183
	v_mul_f32_e32 v31, 0xbfb8aa3b, v31
	v_mul_f32_e32 v32, 0xbfb8aa3b, v32
	v_mul_f32_e32 v181, 0xbfb8aa3b, v181
	v_exp_f32_e32 v180, v180
	v_fma_f32 v29, v4, v182, v184
	v_fmac_f32_e32 v185, v5, v183
	v_exp_f32_e32 v31, v31
	v_exp_f32_e32 v32, v32
	v_exp_f32_e32 v181, v181
	v_mul_f32_e32 v182, 0x3d372713, v22
	v_mul_f32_e32 v183, 0x3d372713, v187
	v_mul_f32_e32 v184, 0x3d372713, v29
	v_mul_f32_e32 v186, 0x3d372713, v185
	v_mul_f32_e32 v182, v22, v182
	v_mul_f32_e32 v183, v187, v183
	v_mul_f32_e32 v184, v29, v184
	v_mul_f32_e32 v186, v185, v186
	v_fma_f32 v182, v22, v182, v22
	v_fma_f32 v183, v187, v183, v187
	v_fma_f32 v184, v29, v184, v29
	v_fma_f32 v186, v185, v186, v185
	v_add_f32_e32 v180, 1.0, v180
	v_mul_f32_e32 v182, 0x3fcc422a, v182
	v_mul_f32_e32 v183, 0x3fcc422a, v183
	v_mul_f32_e32 v184, 0x3fcc422a, v184
	v_mul_f32_e32 v186, 0x3fcc422a, v186
	v_add_f32_e32 v31, 1.0, v31
	v_add_f32_e32 v32, 1.0, v32
	v_add_f32_e32 v181, 1.0, v181
	v_rcp_f32_e32 v180, v180
	v_mul_f32_e32 v182, 0xbfb8aa3b, v182
	v_mul_f32_e32 v183, 0xbfb8aa3b, v183
	v_mul_f32_e32 v184, 0xbfb8aa3b, v184
	v_mul_f32_e32 v186, 0xbfb8aa3b, v186
	v_rcp_f32_e32 v31, v31
	v_rcp_f32_e32 v32, v32
	v_rcp_f32_e32 v181, v181
	v_exp_f32_e32 v182, v182
	v_exp_f32_e32 v183, v183
	v_exp_f32_e32 v184, v184
	v_exp_f32_e32 v186, v186
	v_mul_f32_e32 v14, v14, v180
	v_mul_f32_e32 v13, v13, v31
	v_mul_f32_e32 v31, v33, v32
	v_mul_f32_e32 v23, v23, v181
	v_cvt_pk_bf16_f32 v180, v13, v31
	v_cvt_pk_bf16_f32 v181, v14, v23
	v_lshl_add_u32 v14, v15, 6, v12
	v_add_f32_e32 v182, 1.0, v182
	v_add_f32_e32 v183, 1.0, v183
	v_add_f32_e32 v184, 1.0, v184
	v_add_f32_e32 v186, 1.0, v186
	v_ashrrev_i32_e32 v15, 31, v14
	v_rcp_f32_e32 v182, v182
	v_rcp_f32_e32 v183, v183
	v_rcp_f32_e32 v184, v184
	v_rcp_f32_e32 v186, v186
	v_lshlrev_b64 v[14:15], 10, v[14:15]
	v_lshl_add_u64 v[14:15], s[24:25], 0, v[14:15]
	v_lshl_add_u64 v[14:15], s[2:3], 1, v[14:15]
	v_lshl_add_u64 v[14:15], v[14:15], 0, v[170:171]
	v_mul_f32_e32 v22, v22, v182
	v_mul_f32_e32 v32, v187, v183
	v_mul_f32_e32 v29, v29, v184
	v_mul_f32_e32 v33, v185, v186
	v_cvt_pk_bf16_f32 v182, v22, v32
	v_cvt_pk_bf16_f32 v183, v29, v33
	global_store_dwordx4 v[14:15], v[180:183], off
	s_or_b64 exec, exec, s[20:21]
	s_and_saveexec_b64 s[4:5], s[6:7]
	s_cbranch_execnz .LBB0_561

; #define GAS __attribute__((address_space(1)))
; __device__ __forceinline__ float gelu_tanh(float y) { const float a = 1.5957691216f * (y + 0.044715f * y * y * y); return y * sigmoidf_(a); }
; __device__ __forceinline__ unsigned cvt_pk_bf16(float lo, float hi) { unsigned r; asm volatile("v_cvt_pk_bf16_f32 %0, %1, %2" : "=v"(r) : "v"(lo), "v"(hi)); return r; }
;     __device__ __forceinline__ void operator()(const f32x4 (&acc)[2][2][4][2], const Unit& u, int wr, int wc, int fr, int fq) const {
;     ...
;                 for (int m = 0; m < 4; ++m) { const int inst = inst0 + ai * 128 + m * 16;
;                     if (inst < MT / 64) {
;                         const v4u uu = *(const GAS v4u*)(u2 + ((size_t)(g * NINST + inst) * KS2 + cidx));
;                         const f32x4 a0 = acc[ai][bj][m][0] * S5_INV, a1 = acc[ai][bj][m][1] * S5_INV;
;                         const float y0 = a0[0] + d0[0] * bflo(uu.x), y1 = a0[1] + d0[1] * bfhi(uu.x), y2 = a0[2] + d0[2] * bflo(uu.y), y3 = a0[3] + d0[3] * bfhi(uu.y);
;                         const float y4 = a1[0] + d1[0] * bflo(uu.z), y5 = a1[1] + d1[1] * bfhi(uu.z), y6 = a1[2] + d1[2] * bflo(uu.w), y7 = a1[3] + d1[3] * bfhi(uu.w);
;                         v4u w; w.x = pg8::cvt_pk_bf16(gelu_tanh(y0), gelu_tanh(y1)); w.y = pg8::cvt_pk_bf16(gelu_tanh(y2), gelu_tanh(y3));
;                         w.z = pg8::cvt_pk_bf16(gelu_tanh(y4), gelu_tanh(y5)); w.w = pg8::cvt_pk_bf16(gelu_tanh(y6), gelu_tanh(y7));
;                         *(GAS v4u*)(z + ((size_t)(inst * 64 + t) * DSSM + g * 16 + o0)) = w; } } }
.LBB0_570:
	v_mov_b64_e32 v[14:15], s[22:23]
	v_mad_i64_i32 v[14:15], s[6:7], v25, s66, v[14:15]
	v_lshl_add_u64 v[14:15], v[10:11], 1, v[14:15]
	v_mov_b64_e32 v[22:23], v[166:167]
	v_mov_b64_e32 v[24:25], v[168:169]
	v_pk_mul_f32 v[14:15], v[104:105], s[36:37] op_sel_hi:[1,0]
	v_pk_mul_f32 v[32:33], v[102:103], s[36:37] op_sel_hi:[1,0]
	v_pk_mul_f32 v[180:181], v[100:101], s[36:37] op_sel_hi:[1,0]
	v_pk_mul_f32 v[182:183], v[98:99], s[36:37] op_sel_hi:[1,0]
	s_nop 0
	v_lshlrev_b32_e32 v13, 16, v22
	v_and_b32_e32 v16, 0xffff0000, v22
	v_lshlrev_b32_e32 v22, 16, v23
	v_and_b32_e32 v23, 0xffff0000, v23
	v_lshlrev_b32_e32 v29, 16, v24
	v_and_b32_e32 v24, 0xffff0000, v24
	v_lshlrev_b32_e32 v31, 16, v25
	v_and_b32_e32 v25, 0xffff0000, v25
	v_fma_f32 v13, v6, v13, v32
	v_fmac_f32_e32 v33, v7, v16
	v_fma_f32 v14, v8, v22, v14
	v_fmac_f32_e32 v15, v9, v23
	v_fmac_f32_e32 v183, v3, v24
	v_fma_f32 v22, v4, v31, v180
	v_fmac_f32_e32 v181, v5, v25
	v_mul_f32_e32 v23, 0x3d372713, v13
	v_mul_f32_e32 v24, 0x3d372713, v33
	v_mul_f32_e32 v25, 0x3d372713, v14
	v_fma_f32 v16, v2, v29, v182
	v_mul_f32_e32 v29, 0x3d372713, v15
	v_mul_f32_e32 v180, 0x3d372713, v22
	v_mul_f32_e32 v23, v13, v23
	v_mul_f32_e32 v24, v33, v24
	v_mul_f32_e32 v25, v14, v25
	v_mul_f32_e32 v29, v15, v29
	v_mul_f32_e32 v180, v22, v180
	v_fma_f32 v23, v13, v23, v13
	v_fma_f32 v24, v33, v24, v33
	v_fma_f32 v25, v14, v25, v14
	v_fma_f32 v29, v15, v29, v15
	v_fma_f32 v180, v22, v180, v22
	v_mul_f32_e32 v23, 0x3fcc422a, v23
	v_mul_f32_e32 v24, 0x3fcc422a, v24
	v_mul_f32_e32 v25, 0x3fcc422a, v25
	v_mul_f32_e32 v29, 0x3fcc422a, v29
	v_mul_f32_e32 v180, 0x3fcc422a, v180
	v_mul_f32_e32 v23, 0xbfb8aa3b, v23
	v_mul_f32_e32 v24, 0xbfb8aa3b, v24
	v_mul_f32_e32 v25, 0xbfb8aa3b, v25
	v_mul_f32_e32 v29, 0xbfb8aa3b, v29
	v_mul_f32_e32 v180, 0xbfb8aa3b, v180
	v_exp_f32_e32 v23, v23
	v_exp_f32_e32 v24, v24
	v_exp_f32_e32 v25, v25
	v_mul_f32_e32 v32, 0x3d372713, v183
	v_exp_f32_e32 v29, v29
	v_exp_f32_e32 v180, v180
	v_mul_f32_e32 v31, 0x3d372713, v16
	v_mul_f32_e32 v182, 0x3d372713, v181
	v_mul_f32_e32 v32, v183, v32
	v_mul_f32_e32 v31, v16, v31
	v_mul_f32_e32 v182, v181, v182
	v_fma_f32 v32, v183, v32, v183
	v_fma_f32 v31, v16, v31, v16
	v_fma_f32 v182, v181, v182, v181
	v_mul_f32_e32 v32, 0x3fcc422a, v32
	v_add_f32_e32 v23, 1.0, v23
	v_add_f32_e32 v24, 1.0, v24
	v_add_f32_e32 v25, 1.0, v25
	v_mul_f32_e32 v31, 0x3fcc422a, v31
	v_mul_f32_e32 v182, 0x3fcc422a, v182
	v_mul_f32_e32 v32, 0xbfb8aa3b, v32
	v_add_f32_e32 v29, 1.0, v29
	v_add_f32_e32 v180, 1.0, v180
	v_rcp_f32_e32 v23, v23
	v_rcp_f32_e32 v24, v24
	v_rcp_f32_e32 v25, v25
	v_mul_f32_e32 v31, 0xbfb8aa3b, v31
	v_mul_f32_e32 v182, 0xbfb8aa3b, v182
	v_exp_f32_e32 v32, v32
	v_rcp_f32_e32 v29, v29
	v_rcp_f32_e32 v180, v180
	v_exp_f32_e32 v31, v31
	v_exp_f32_e32 v182, v182
	v_mul_f32_e32 v13, v13, v23
	v_mul_f32_e32 v23, v33, v24
	v_mul_f32_e32 v14, v14, v25
	v_add_f32_e32 v32, 1.0, v32
	v_mul_f32_e32 v15, v15, v29
	v_mul_f32_e32 v25, v22, v180
	v_cvt_pk_bf16_f32 v22, v13, v23
	v_cvt_pk_bf16_f32 v23, v14, v15
	v_lshl_add_u32 v14, v17, 6, v12
	v_add_f32_e32 v31, 1.0, v31
	v_add_f32_e32 v182, 1.0, v182
	v_rcp_f32_e32 v32, v32
	v_ashrrev_i32_e32 v15, 31, v14
	v_rcp_f32_e32 v31, v31
	v_rcp_f32_e32 v182, v182
	v_lshlrev_b64 v[14:15], 10, v[14:15]
	v_lshl_add_u64 v[14:15], s[24:25], 0, v[14:15]
	v_lshl_add_u64 v[14:15], s[2:3], 1, v[14:15]
	v_mul_f32_e32 v24, v183, v32
	v_lshl_add_u64 v[14:15], v[14:15], 0, v[170:171]
	v_mul_f32_e32 v16, v16, v31
	v_mul_f32_e32 v29, v181, v182
	v_cvt_pk_bf16_f32 v24, v16, v24
	v_cvt_pk_bf16_f32 v25, v25, v29
	global_store_dwordx4 v[14:15], v[22:25], off
	s_or_b64 exec, exec, s[4:5]
	s_and_saveexec_b64 s[4:5], s[10:11]
	s_cbranch_execnz .LBB0_563

; #define GAS __attribute__((address_space(1)))
; __device__ __forceinline__ float gelu_tanh(float y) { const float a = 1.5957691216f * (y + 0.044715f * y * y * y); return y * sigmoidf_(a); }
; __device__ __forceinline__ unsigned cvt_pk_bf16(float lo, float hi) { unsigned r; asm volatile("v_cvt_pk_bf16_f32 %0, %1, %2" : "=v"(r) : "v"(lo), "v"(hi)); return r; }
;     __device__ __forceinline__ void operator()(const f32x4 (&acc)[2][2][4][2], const Unit& u, int wr, int wc, int fr, int fq) const {
;     ...
;                 for (int m = 0; m < 4; ++m) { const int inst = inst0 + ai * 128 + m * 16;
;                     if (inst < MT / 64) {
;                         const v4u uu = *(const GAS v4u*)(u2 + ((size_t)(g * NINST + inst) * KS2 + cidx));
;                         const f32x4 a0 = acc[ai][bj][m][0] * S5_INV, a1 = acc[ai][bj][m][1] * S5_INV;
;                         const float y0 = a0[0] + d0[0] * bflo(uu.x), y1 = a0[1] + d0[1] * bfhi(uu.x), y2 = a0[2] + d0[2] * bflo(uu.y), y3 = a0[3] + d0[3] * bfhi(uu.y);
;                         const float y4 = a1[0] + d1[0] * bflo(uu.z), y5 = a1[1] + d1[1] * bfhi(uu.z), y6 = a1[2] + d1[2] * bflo(uu.w), y7 = a1[3] + d1[3] * bfhi(uu.w);
;                         v4u w; w.x = pg8::cvt_pk_bf16(gelu_tanh(y0), gelu_tanh(y1)); w.y = pg8::cvt_pk_bf16(gelu_tanh(y2), gelu_tanh(y3));
;                         w.z = pg8::cvt_pk_bf16(gelu_tanh(y4), gelu_tanh(y5)); w.w = pg8::cvt_pk_bf16(gelu_tanh(y6), gelu_tanh(y7));
;                         *(GAS v4u*)(z + ((size_t)(inst * 64 + t) * DSSM + g * 16 + o0)) = w; } } }
.LBB0_572:
	v_mov_b64_e32 v[14:15], s[22:23]
	v_mad_i64_i32 v[14:15], s[6:7], v27, s66, v[14:15]
	v_lshl_add_u64 v[14:15], v[10:11], 1, v[14:15]
	v_mov_b64_e32 v[14:15], v[176:177]
	v_mov_b64_e32 v[16:17], v[178:179]
	v_pk_mul_f32 v[22:23], v[56:57], s[36:37] op_sel_hi:[1,0]
	v_pk_mul_f32 v[24:25], v[54:55], s[36:37] op_sel_hi:[1,0]
	v_pk_mul_f32 v[26:27], v[52:53], s[36:37] op_sel_hi:[1,0]
	v_pk_mul_f32 v[32:33], v[50:51], s[36:37] op_sel_hi:[1,0]
	s_nop 0
	v_lshlrev_b32_e32 v13, 16, v14
	v_and_b32_e32 v14, 0xffff0000, v14
	v_lshlrev_b32_e32 v18, 16, v15
	v_and_b32_e32 v15, 0xffff0000, v15
	v_lshlrev_b32_e32 v29, 16, v16
	v_lshlrev_b32_e32 v31, 16, v17
	v_and_b32_e32 v17, 0xffff0000, v17
	v_fma_f32 v13, v6, v13, v24
	v_fmac_f32_e32 v25, v7, v14
	v_fma_f32 v14, v8, v18, v22
	v_and_b32_e32 v16, 0xffff0000, v16
	v_fmac_f32_e32 v23, v9, v15
	v_fma_f32 v15, v2, v29, v32
	v_fmac_f32_e32 v27, v5, v17
	v_mul_f32_e32 v17, 0x3d372713, v13
	v_mul_f32_e32 v18, 0x3d372713, v25
	v_mul_f32_e32 v22, 0x3d372713, v14
	v_fmac_f32_e32 v33, v3, v16
	v_fma_f32 v16, v4, v31, v26
	v_mul_f32_e32 v24, 0x3d372713, v23
	v_mul_f32_e32 v26, 0x3d372713, v15
	v_mul_f32_e32 v17, v13, v17
	v_mul_f32_e32 v18, v25, v18
	v_mul_f32_e32 v22, v14, v22
	v_mul_f32_e32 v24, v23, v24
	v_mul_f32_e32 v26, v15, v26
	v_fma_f32 v17, v13, v17, v13
	v_fma_f32 v18, v25, v18, v25
	v_fma_f32 v22, v14, v22, v14
	v_fma_f32 v24, v23, v24, v23
	v_fma_f32 v26, v15, v26, v15
	v_mul_f32_e32 v17, 0x3fcc422a, v17
	v_mul_f32_e32 v18, 0x3fcc422a, v18
	v_mul_f32_e32 v22, 0x3fcc422a, v22
	v_mul_f32_e32 v24, 0x3fcc422a, v24
	v_mul_f32_e32 v26, 0x3fcc422a, v26
	v_mul_f32_e32 v17, 0xbfb8aa3b, v17
	v_mul_f32_e32 v18, 0xbfb8aa3b, v18
	v_mul_f32_e32 v22, 0xbfb8aa3b, v22
	v_mul_f32_e32 v24, 0xbfb8aa3b, v24
	v_mul_f32_e32 v26, 0xbfb8aa3b, v26
	v_exp_f32_e32 v17, v17
	v_exp_f32_e32 v18, v18
	v_exp_f32_e32 v22, v22
	v_exp_f32_e32 v24, v24
	v_exp_f32_e32 v26, v26
	v_mul_f32_e32 v29, 0x3d372713, v33
	v_mul_f32_e32 v31, 0x3d372713, v16
	v_mul_f32_e32 v32, 0x3d372713, v27
	v_mul_f32_e32 v29, v33, v29
	v_mul_f32_e32 v31, v16, v31
	v_mul_f32_e32 v32, v27, v32
	v_fma_f32 v29, v33, v29, v33
	v_fma_f32 v31, v16, v31, v16
	v_fma_f32 v32, v27, v32, v27
	v_add_f32_e32 v17, 1.0, v17
	v_add_f32_e32 v18, 1.0, v18
	v_add_f32_e32 v22, 1.0, v22
	v_mul_f32_e32 v29, 0x3fcc422a, v29
	v_mul_f32_e32 v31, 0x3fcc422a, v31
	v_mul_f32_e32 v32, 0x3fcc422a, v32
	v_add_f32_e32 v24, 1.0, v24
	v_add_f32_e32 v26, 1.0, v26
	v_rcp_f32_e32 v17, v17
	v_rcp_f32_e32 v18, v18
	v_rcp_f32_e32 v22, v22
	v_mul_f32_e32 v29, 0xbfb8aa3b, v29
	v_mul_f32_e32 v31, 0xbfb8aa3b, v31
	v_mul_f32_e32 v32, 0xbfb8aa3b, v32
	v_rcp_f32_e32 v24, v24
	v_rcp_f32_e32 v26, v26
	v_exp_f32_e32 v29, v29
	v_exp_f32_e32 v31, v31
	v_exp_f32_e32 v32, v32
	v_mul_f32_e32 v13, v13, v17
	v_mul_f32_e32 v17, v25, v18
	v_mul_f32_e32 v18, v14, v22
	v_mul_f32_e32 v22, v23, v24
	v_mul_f32_e32 v23, v15, v26
	v_cvt_pk_bf16_f32 v14, v13, v17
	v_cvt_pk_bf16_f32 v15, v18, v22
	v_lshl_add_u32 v18, v19, 6, v12
	v_add_f32_e32 v29, 1.0, v29
	v_add_f32_e32 v31, 1.0, v31
	v_add_f32_e32 v32, 1.0, v32
	v_ashrrev_i32_e32 v19, 31, v18
	v_rcp_f32_e32 v29, v29
	v_rcp_f32_e32 v31, v31
	v_rcp_f32_e32 v32, v32
	v_lshlrev_b64 v[18:19], 10, v[18:19]
	v_lshl_add_u64 v[18:19], s[24:25], 0, v[18:19]
	v_lshl_add_u64 v[18:19], s[2:3], 1, v[18:19]
	v_lshl_add_u64 v[18:19], v[18:19], 0, v[170:171]
	v_mul_f32_e32 v24, v33, v29
	v_mul_f32_e32 v25, v16, v31
	v_mul_f32_e32 v26, v27, v32
	v_cvt_pk_bf16_f32 v16, v23, v24
	v_cvt_pk_bf16_f32 v17, v25, v26
	global_store_dwordx4 v[18:19], v[14:17], off
	s_or_b64 exec, exec, s[4:5]
	s_and_saveexec_b64 s[4:5], s[14:15]
	s_cbranch_execnz .LBB0_565

; #define GAS __attribute__((address_space(1)))
; __device__ __forceinline__ float gelu_tanh(float y) { const float a = 1.5957691216f * (y + 0.044715f * y * y * y); return y * sigmoidf_(a); }
; __device__ __forceinline__ unsigned cvt_pk_bf16(float lo, float hi) { unsigned r; asm volatile("v_cvt_pk_bf16_f32 %0, %1, %2" : "=v"(r) : "v"(lo), "v"(hi)); return r; }
;     __device__ __forceinline__ void operator()(const f32x4 (&acc)[2][2][4][2], const Unit& u, int wr, int wc, int fr, int fq) const {
;     ...
;                 for (int m = 0; m < 4; ++m) { const int inst = inst0 + ai * 128 + m * 16;
;                     if (inst < MT / 64) {
;                         const v4u uu = *(const GAS v4u*)(u2 + ((size_t)(g * NINST + inst) * KS2 + cidx));
;                         const f32x4 a0 = acc[ai][bj][m][0] * S5_INV, a1 = acc[ai][bj][m][1] * S5_INV;
;                         const float y0 = a0[0] + d0[0] * bflo(uu.x), y1 = a0[1] + d0[1] * bfhi(uu.x), y2 = a0[2] + d0[2] * bflo(uu.y), y3 = a0[3] + d0[3] * bfhi(uu.y);
;                         const float y4 = a1[0] + d1[0] * bflo(uu.z), y5 = a1[1] + d1[1] * bfhi(uu.z), y6 = a1[2] + d1[2] * bflo(uu.w), y7 = a1[3] + d1[3] * bfhi(uu.w);
;                         v4u w; w.x = pg8::cvt_pk_bf16(gelu_tanh(y0), gelu_tanh(y1)); w.y = pg8::cvt_pk_bf16(gelu_tanh(y2), gelu_tanh(y3));
;                         w.z = pg8::cvt_pk_bf16(gelu_tanh(y4), gelu_tanh(y5)); w.w = pg8::cvt_pk_bf16(gelu_tanh(y6), gelu_tanh(y7));
;                         *(GAS v4u*)(z + ((size_t)(inst * 64 + t) * DSSM + g * 16 + o0)) = w; } } }
.LBB0_574:
	v_mov_b64_e32 v[14:15], s[22:23]
	v_mad_i64_i32 v[14:15], s[6:7], v30, s66, v[14:15]
	v_lshl_add_u64 v[10:11], v[10:11], 1, v[14:15]
	v_mov_b64_e32 v[14:15], v[250:251]
	v_mov_b64_e32 v[16:17], v[252:253]
	v_pk_mul_f32 v[10:11], v[40:41], s[36:37] op_sel_hi:[1,0]
	v_pk_mul_f32 v[18:19], v[38:39], s[36:37] op_sel_hi:[1,0]
	v_pk_mul_f32 v[22:23], v[36:37], s[36:37] op_sel_hi:[1,0]
	v_pk_mul_f32 v[24:25], v[34:35], s[36:37] op_sel_hi:[1,0]
	s_nop 0
	v_lshlrev_b32_e32 v13, 16, v14
	v_and_b32_e32 v14, 0xffff0000, v14
	v_lshlrev_b32_e32 v20, 16, v15
	v_and_b32_e32 v15, 0xffff0000, v15
	v_lshlrev_b32_e32 v26, 16, v16
	v_and_b32_e32 v16, 0xffff0000, v16
	v_lshlrev_b32_e32 v27, 16, v17
	v_fma_f32 v6, v6, v13, v18
	v_fmac_f32_e32 v19, v7, v14
	v_fma_f32 v7, v8, v20, v10
	v_and_b32_e32 v17, 0xffff0000, v17
	v_fmac_f32_e32 v11, v9, v15
	v_fma_f32 v2, v2, v26, v24
	v_fmac_f32_e32 v25, v3, v16
	v_fma_f32 v3, v4, v27, v22
	v_mul_f32_e32 v4, 0x3d372713, v6
	v_mul_f32_e32 v8, 0x3d372713, v7
	v_fmac_f32_e32 v23, v5, v17
	v_mul_f32_e32 v5, 0x3d372713, v19
	v_mul_f32_e32 v9, 0x3d372713, v11
	v_mul_f32_e32 v10, 0x3d372713, v2
	v_mul_f32_e32 v14, 0x3d372713, v3
	v_mul_f32_e32 v4, v6, v4
	v_mul_f32_e32 v8, v7, v8
	v_mul_f32_e32 v5, v19, v5
	v_mul_f32_e32 v9, v11, v9
	v_mul_f32_e32 v10, v2, v10
	v_mul_f32_e32 v14, v3, v14
	v_fma_f32 v4, v6, v4, v6
	v_fma_f32 v8, v7, v8, v7
	v_fma_f32 v5, v19, v5, v19
	v_fma_f32 v9, v11, v9, v11
	v_fma_f32 v10, v2, v10, v2
	v_fma_f32 v14, v3, v14, v3
	v_mul_f32_e32 v4, 0x3fcc422a, v4
	v_mul_f32_e32 v8, 0x3fcc422a, v8
	v_mul_f32_e32 v5, 0x3fcc422a, v5
	v_mul_f32_e32 v9, 0x3fcc422a, v9
	v_mul_f32_e32 v10, 0x3fcc422a, v10
	v_mul_f32_e32 v14, 0x3fcc422a, v14
	v_mul_f32_e32 v4, 0xbfb8aa3b, v4
	v_mul_f32_e32 v8, 0xbfb8aa3b, v8
	v_mul_f32_e32 v5, 0xbfb8aa3b, v5
	v_mul_f32_e32 v9, 0xbfb8aa3b, v9
	v_mul_f32_e32 v10, 0xbfb8aa3b, v10
	v_mul_f32_e32 v14, 0xbfb8aa3b, v14
	v_exp_f32_e32 v4, v4
	v_exp_f32_e32 v8, v8
	v_exp_f32_e32 v5, v5
	v_exp_f32_e32 v9, v9
	v_exp_f32_e32 v10, v10
	v_exp_f32_e32 v14, v14
	v_mul_f32_e32 v13, 0x3d372713, v25
	v_mul_f32_e32 v15, 0x3d372713, v23
	v_mul_f32_e32 v13, v25, v13
	v_mul_f32_e32 v15, v23, v15
	v_fma_f32 v13, v25, v13, v25
	v_fma_f32 v15, v23, v15, v23
	v_add_f32_e32 v4, 1.0, v4
	v_add_f32_e32 v8, 1.0, v8
	v_mul_f32_e32 v13, 0x3fcc422a, v13
	v_mul_f32_e32 v15, 0x3fcc422a, v15
	v_add_f32_e32 v5, 1.0, v5
	v_add_f32_e32 v9, 1.0, v9
	v_add_f32_e32 v10, 1.0, v10
	v_add_f32_e32 v14, 1.0, v14
	v_rcp_f32_e32 v4, v4
	v_rcp_f32_e32 v8, v8
	v_mul_f32_e32 v13, 0xbfb8aa3b, v13
	v_mul_f32_e32 v15, 0xbfb8aa3b, v15
	v_rcp_f32_e32 v5, v5
	v_rcp_f32_e32 v9, v9
	v_rcp_f32_e32 v10, v10
	v_rcp_f32_e32 v14, v14
	v_exp_f32_e32 v13, v13
	v_exp_f32_e32 v15, v15
	v_mul_f32_e32 v4, v6, v4
	v_mul_f32_e32 v6, v7, v8
	v_mul_f32_e32 v5, v19, v5
	v_mul_f32_e32 v7, v11, v9
	v_mul_f32_e32 v8, v2, v10
	v_mul_f32_e32 v10, v3, v14
	v_cvt_pk_bf16_f32 v2, v4, v5
	v_cvt_pk_bf16_f32 v3, v6, v7
	v_lshl_add_u32 v6, v21, 6, v12
	v_add_f32_e32 v13, 1.0, v13
	v_add_f32_e32 v15, 1.0, v15
	v_ashrrev_i32_e32 v7, 31, v6
	v_rcp_f32_e32 v13, v13
	v_rcp_f32_e32 v15, v15
	v_lshlrev_b64 v[6:7], 10, v[6:7]
	v_lshl_add_u64 v[6:7], s[24:25], 0, v[6:7]
	v_lshl_add_u64 v[6:7], s[2:3], 1, v[6:7]
	v_lshl_add_u64 v[6:7], v[6:7], 0, v[170:171]
	v_mul_f32_e32 v9, v25, v13
	v_mul_f32_e32 v11, v23, v15
	v_cvt_pk_bf16_f32 v4, v8, v9
	v_cvt_pk_bf16_f32 v5, v10, v11
	global_store_dwordx4 v[6:7], v[2:5], off
	s_or_b64 exec, exec, s[4:5]
	s_andn2_b64 vcc, exec, s[40:41]
	s_mov_b64 s[2:3], -1
	s_cbranch_vccnz .LBB0_535

; template <int LO, int HI>
; __global__ void __launch_bounds__(NWAVES * 64, 2) trunk_fwd(Args args) {
	.amdhsa_kernel _Z9trunk_fwdILi0ELi24EEv4Args
		.amdhsa_group_segment_fixed_size 0
		.amdhsa_private_segment_fixed_size 0
		.amdhsa_kernarg_size 488
		.amdhsa_user_sgpr_count 2
		.amdhsa_user_sgpr_dispatch_ptr 0
		.amdhsa_user_sgpr_queue_ptr 0
		.amdhsa_user_sgpr_kernarg_segment_ptr 1
		.amdhsa_user_sgpr_dispatch_id 0
		.amdhsa_user_sgpr_kernarg_preload_length 0
		.amdhsa_user_sgpr_kernarg_preload_offset 0
		.amdhsa_user_sgpr_private_segment_size 0
		.amdhsa_uses_dynamic_stack 0
		.amdhsa_enable_private_segment 0
		.amdhsa_system_sgpr_workgroup_id_x 1
		.amdhsa_system_sgpr_workgroup_id_y 0
		.amdhsa_system_sgpr_workgroup_id_z 0
		.amdhsa_system_sgpr_workgroup_info 0
		.amdhsa_system_vgpr_workitem_id 0
		.amdhsa_next_free_vgpr 256
		.amdhsa_next_free_sgpr 102
		.amdhsa_accum_offset 256
		.amdhsa_reserve_vcc 1
		.amdhsa_float_round_mode_32 0
		.amdhsa_float_round_mode_16_64 0
		.amdhsa_float_denorm_mode_32 3
		.amdhsa_float_denorm_mode_16_64 3
		.amdhsa_dx10_clamp 1
		.amdhsa_ieee_mode 1
		.amdhsa_fp16_overflow 0
		.amdhsa_tg_split 0
		.amdhsa_exception_fp_ieee_invalid_op 0
		.amdhsa_exception_fp_denorm_src 0
		.amdhsa_exception_fp_ieee_div_zero 0
		.amdhsa_exception_fp_ieee_overflow 0
		.amdhsa_exception_fp_ieee_underflow 0
		.amdhsa_exception_fp_ieee_inexact 0
		.amdhsa_exception_int_div_zero 0
	.end_amdhsa_kernel

; template <int LO, int HI>
; __global__ void __launch_bounds__(NWAVES * 64, 2) trunk_fwd(Args args) {
amdhsa.kernels:
  - .agpr_count:     0
    .args:
      - .offset:         0
        .size:           232
        .value_kind:     by_value
      - .offset:         232
        .size:           4
        .value_kind:     hidden_block_count_x
      - .offset:         236
        .size:           4
        .value_kind:     hidden_block_count_y
      - .offset:         240
        .size:           4
        .value_kind:     hidden_block_count_z
      - .offset:         244
        .size:           2
        .value_kind:     hidden_group_size_x
      - .offset:         246
        .size:           2
        .value_kind:     hidden_group_size_y
      - .offset:         248
        .size:           2
        .value_kind:     hidden_group_size_z
      - .offset:         250
        .size:           2
        .value_kind:     hidden_remainder_x
      - .offset:         252
        .size:           2
        .value_kind:     hidden_remainder_y
      - .offset:         254
        .size:           2
        .value_kind:     hidden_remainder_z
      - .offset:         272
        .size:           8
        .value_kind:     hidden_global_offset_x
      - .offset:         280
        .size:           8
        .value_kind:     hidden_global_offset_y
      - .offset:         288
        .size:           8
        .value_kind:     hidden_global_offset_z
      - .offset:         296
        .size:           2
        .value_kind:     hidden_grid_dims
      - .offset:         352
        .size:           4
        .value_kind:     hidden_dynamic_lds_size
    .group_segment_fixed_size: 0
    .kernarg_segment_align: 8
    .kernarg_segment_size: 488
    .language:       OpenCL C
    .language_version:
      - 2
      - 0
    .max_flat_workgroup_size: 512
    .name:           _Z9trunk_fwdILi0ELi24EEv4Args
    .private_segment_fixed_size: 0
    .sgpr_count:     108
    .sgpr_spill_count: 30
    .symbol:         _Z9trunk_fwdILi0ELi24EEv4Args.kd
    .uniform_work_group_size: 1
    .uses_dynamic_stack: false
    .vgpr_count:     256
    .vgpr_spill_count: 0
    .wavefront_size: 64
